# PEER tail: the token's x1 row loads and the output row stores marked non-temporal (streamed once; keeps the expert tables in cache)
# speedup vs baseline: 1.0048x; 1.0037x over previous
.Lpv_loop:
	ds_read_b128 v[212:215], v102 offset:32
	ds_read_b128 v[216:219], v102 offset:512
	s_waitcnt lgkmcnt(0)
	s_waitcnt vmcnt(14)
	v_cvt_scalef32_pk_f32_fp4 v[220:221], v148, 1.0
	v_pk_fma_f32 v[96:97], v[220:221], v[216:217], v[96:97] op_sel_hi:[1,0,1]
	v_cvt_scalef32_pk_f32_fp4 v[222:223], v148, 1.0 op_sel:[1,0,0]
	v_pk_fma_f32 v[98:99], v[222:223], v[216:217], v[98:99] op_sel_hi:[1,0,1]
	v_cvt_scalef32_pk_f32_fp4 v[224:225], v148, 1.0 op_sel:[0,1,0]
	v_pk_fma_f32 v[94:95], v[224:225], v[216:217], v[94:95] op_sel_hi:[1,0,1]
	v_cvt_scalef32_pk_f32_fp4 v[226:227], v148, 1.0 op_sel:[1,1,0]
	v_pk_fma_f32 v[92:93], v[226:227], v[216:217], v[92:93] op_sel_hi:[1,0,1]
	v_cvt_scalef32_pk_f32_fp4 v[220:221], v149, 1.0
	v_pk_fma_f32 v[90:91], v[220:221], v[216:217], v[90:91] op_sel_hi:[1,0,1]
	v_cvt_scalef32_pk_f32_fp4 v[222:223], v149, 1.0 op_sel:[1,0,0]
	v_pk_fma_f32 v[88:89], v[222:223], v[216:217], v[88:89] op_sel_hi:[1,0,1]
	v_cvt_scalef32_pk_f32_fp4 v[224:225], v149, 1.0 op_sel:[0,1,0]
	v_pk_fma_f32 v[86:87], v[224:225], v[216:217], v[86:87] op_sel_hi:[1,0,1]
	v_cvt_scalef32_pk_f32_fp4 v[226:227], v149, 1.0 op_sel:[1,1,0]
	v_pk_fma_f32 v[84:85], v[226:227], v[216:217], v[84:85] op_sel_hi:[1,0,1]
	v_cvt_scalef32_pk_f32_fp4 v[220:221], v150, 1.0
	v_pk_fma_f32 v[82:83], v[220:221], v[216:217], v[82:83] op_sel_hi:[1,0,1]
	v_cvt_scalef32_pk_f32_fp4 v[222:223], v150, 1.0 op_sel:[1,0,0]
	v_pk_fma_f32 v[80:81], v[222:223], v[216:217], v[80:81] op_sel_hi:[1,0,1]
	v_cvt_scalef32_pk_f32_fp4 v[224:225], v150, 1.0 op_sel:[0,1,0]
	v_pk_fma_f32 v[78:79], v[224:225], v[216:217], v[78:79] op_sel_hi:[1,0,1]
	v_cvt_scalef32_pk_f32_fp4 v[226:227], v150, 1.0 op_sel:[1,1,0]
	v_pk_fma_f32 v[76:77], v[226:227], v[216:217], v[76:77] op_sel_hi:[1,0,1]
	v_cvt_scalef32_pk_f32_fp4 v[220:221], v151, 1.0
	v_pk_fma_f32 v[74:75], v[220:221], v[216:217], v[74:75] op_sel_hi:[1,0,1]
	v_cvt_scalef32_pk_f32_fp4 v[222:223], v151, 1.0 op_sel:[1,0,0]
	v_pk_fma_f32 v[72:73], v[222:223], v[216:217], v[72:73] op_sel_hi:[1,0,1]
	v_cvt_scalef32_pk_f32_fp4 v[224:225], v151, 1.0 op_sel:[0,1,0]
	v_pk_fma_f32 v[70:71], v[224:225], v[216:217], v[70:71] op_sel_hi:[1,0,1]
	v_cvt_scalef32_pk_f32_fp4 v[226:227], v151, 1.0 op_sel:[1,1,0]
	v_pk_fma_f32 v[68:69], v[226:227], v[216:217], v[68:69] op_sel_hi:[1,0,1]
	v_cvt_scalef32_pk_f32_fp4 v[220:221], v152, 1.0
	v_pk_fma_f32 v[66:67], v[220:221], v[216:217], v[66:67] op_sel_hi:[1,0,1]
	v_cvt_scalef32_pk_f32_fp4 v[222:223], v152, 1.0 op_sel:[1,0,0]
	v_pk_fma_f32 v[64:65], v[222:223], v[216:217], v[64:65] op_sel_hi:[1,0,1]
	v_cvt_scalef32_pk_f32_fp4 v[224:225], v152, 1.0 op_sel:[0,1,0]
	v_pk_fma_f32 v[62:63], v[224:225], v[216:217], v[62:63] op_sel_hi:[1,0,1]
	v_cvt_scalef32_pk_f32_fp4 v[226:227], v152, 1.0 op_sel:[1,1,0]
	v_pk_fma_f32 v[60:61], v[226:227], v[216:217], v[60:61] op_sel_hi:[1,0,1]
	v_cvt_scalef32_pk_f32_fp4 v[220:221], v153, 1.0
	v_pk_fma_f32 v[58:59], v[220:221], v[216:217], v[58:59] op_sel_hi:[1,0,1]
	v_cvt_scalef32_pk_f32_fp4 v[222:223], v153, 1.0 op_sel:[1,0,0]
	v_pk_fma_f32 v[56:57], v[222:223], v[216:217], v[56:57] op_sel_hi:[1,0,1]
	v_cvt_scalef32_pk_f32_fp4 v[224:225], v153, 1.0 op_sel:[0,1,0]
	v_pk_fma_f32 v[54:55], v[224:225], v[216:217], v[54:55] op_sel_hi:[1,0,1]
	v_cvt_scalef32_pk_f32_fp4 v[226:227], v153, 1.0 op_sel:[1,1,0]
	v_pk_fma_f32 v[52:53], v[226:227], v[216:217], v[52:53] op_sel_hi:[1,0,1]
	v_cvt_scalef32_pk_f32_fp4 v[220:221], v154, 1.0
	v_pk_fma_f32 v[50:51], v[220:221], v[216:217], v[50:51] op_sel_hi:[1,0,1]
	v_cvt_scalef32_pk_f32_fp4 v[222:223], v154, 1.0 op_sel:[1,0,0]
	v_pk_fma_f32 v[46:47], v[222:223], v[216:217], v[46:47] op_sel_hi:[1,0,1]
	v_cvt_scalef32_pk_f32_fp4 v[224:225], v154, 1.0 op_sel:[0,1,0]
	v_pk_fma_f32 v[44:45], v[224:225], v[216:217], v[44:45] op_sel_hi:[1,0,1]
	v_cvt_scalef32_pk_f32_fp4 v[226:227], v154, 1.0 op_sel:[1,1,0]
	v_pk_fma_f32 v[42:43], v[226:227], v[216:217], v[42:43] op_sel_hi:[1,0,1]
	v_cvt_scalef32_pk_f32_fp4 v[220:221], v155, 1.0
	v_pk_fma_f32 v[40:41], v[220:221], v[216:217], v[40:41] op_sel_hi:[1,0,1]
	v_cvt_scalef32_pk_f32_fp4 v[222:223], v155, 1.0 op_sel:[1,0,0]
	v_pk_fma_f32 v[38:39], v[222:223], v[216:217], v[38:39] op_sel_hi:[1,0,1]
	v_cvt_scalef32_pk_f32_fp4 v[224:225], v155, 1.0 op_sel:[0,1,0]
	v_pk_fma_f32 v[36:37], v[224:225], v[216:217], v[36:37] op_sel_hi:[1,0,1]
	v_cvt_scalef32_pk_f32_fp4 v[226:227], v155, 1.0 op_sel:[1,1,0]
	v_pk_fma_f32 v[34:35], v[226:227], v[216:217], v[34:35] op_sel_hi:[1,0,1]
	s_waitcnt vmcnt(12)
	v_cvt_scalef32_pk_f32_fp4 v[220:221], v156, 1.0
	v_pk_fma_f32 v[96:97], v[220:221], v[216:217], v[96:97] op_sel:[0,1,0] op_sel_hi:[1,1,1]
	v_cvt_scalef32_pk_f32_fp4 v[222:223], v156, 1.0 op_sel:[1,0,0]
	v_pk_fma_f32 v[98:99], v[222:223], v[216:217], v[98:99] op_sel:[0,1,0] op_sel_hi:[1,1,1]
	v_cvt_scalef32_pk_f32_fp4 v[224:225], v156, 1.0 op_sel:[0,1,0]
	v_pk_fma_f32 v[94:95], v[224:225], v[216:217], v[94:95] op_sel:[0,1,0] op_sel_hi:[1,1,1]
	v_cvt_scalef32_pk_f32_fp4 v[226:227], v156, 1.0 op_sel:[1,1,0]
	v_pk_fma_f32 v[92:93], v[226:227], v[216:217], v[92:93] op_sel:[0,1,0] op_sel_hi:[1,1,1]
	v_cvt_scalef32_pk_f32_fp4 v[220:221], v157, 1.0
	v_pk_fma_f32 v[90:91], v[220:221], v[216:217], v[90:91] op_sel:[0,1,0] op_sel_hi:[1,1,1]
	v_cvt_scalef32_pk_f32_fp4 v[222:223], v157, 1.0 op_sel:[1,0,0]
	v_pk_fma_f32 v[88:89], v[222:223], v[216:217], v[88:89] op_sel:[0,1,0] op_sel_hi:[1,1,1]
	v_cvt_scalef32_pk_f32_fp4 v[224:225], v157, 1.0 op_sel:[0,1,0]
	v_pk_fma_f32 v[86:87], v[224:225], v[216:217], v[86:87] op_sel:[0,1,0] op_sel_hi:[1,1,1]
	v_cvt_scalef32_pk_f32_fp4 v[226:227], v157, 1.0 op_sel:[1,1,0]
	v_pk_fma_f32 v[84:85], v[226:227], v[216:217], v[84:85] op_sel:[0,1,0] op_sel_hi:[1,1,1]
	v_cvt_scalef32_pk_f32_fp4 v[220:221], v158, 1.0
	v_pk_fma_f32 v[82:83], v[220:221], v[216:217], v[82:83] op_sel:[0,1,0] op_sel_hi:[1,1,1]
	v_cvt_scalef32_pk_f32_fp4 v[222:223], v158, 1.0 op_sel:[1,0,0]
	v_pk_fma_f32 v[80:81], v[222:223], v[216:217], v[80:81] op_sel:[0,1,0] op_sel_hi:[1,1,1]
	v_cvt_scalef32_pk_f32_fp4 v[224:225], v158, 1.0 op_sel:[0,1,0]
	v_pk_fma_f32 v[78:79], v[224:225], v[216:217], v[78:79] op_sel:[0,1,0] op_sel_hi:[1,1,1]
	v_cvt_scalef32_pk_f32_fp4 v[226:227], v158, 1.0 op_sel:[1,1,0]
	v_pk_fma_f32 v[76:77], v[226:227], v[216:217], v[76:77] op_sel:[0,1,0] op_sel_hi:[1,1,1]
	v_cvt_scalef32_pk_f32_fp4 v[220:221], v159, 1.0
	v_pk_fma_f32 v[74:75], v[220:221], v[216:217], v[74:75] op_sel:[0,1,0] op_sel_hi:[1,1,1]
	v_cvt_scalef32_pk_f32_fp4 v[222:223], v159, 1.0 op_sel:[1,0,0]
	v_pk_fma_f32 v[72:73], v[222:223], v[216:217], v[72:73] op_sel:[0,1,0] op_sel_hi:[1,1,1]
	v_cvt_scalef32_pk_f32_fp4 v[224:225], v159, 1.0 op_sel:[0,1,0]
	v_pk_fma_f32 v[70:71], v[224:225], v[216:217], v[70:71] op_sel:[0,1,0] op_sel_hi:[1,1,1]
	v_cvt_scalef32_pk_f32_fp4 v[226:227], v159, 1.0 op_sel:[1,1,0]
	v_pk_fma_f32 v[68:69], v[226:227], v[216:217], v[68:69] op_sel:[0,1,0] op_sel_hi:[1,1,1]
	v_cvt_scalef32_pk_f32_fp4 v[220:221], v160, 1.0
	v_pk_fma_f32 v[66:67], v[220:221], v[216:217], v[66:67] op_sel:[0,1,0] op_sel_hi:[1,1,1]
	v_cvt_scalef32_pk_f32_fp4 v[222:223], v160, 1.0 op_sel:[1,0,0]
	v_pk_fma_f32 v[64:65], v[222:223], v[216:217], v[64:65] op_sel:[0,1,0] op_sel_hi:[1,1,1]
	v_cvt_scalef32_pk_f32_fp4 v[224:225], v160, 1.0 op_sel:[0,1,0]
	v_pk_fma_f32 v[62:63], v[224:225], v[216:217], v[62:63] op_sel:[0,1,0] op_sel_hi:[1,1,1]
	v_cvt_scalef32_pk_f32_fp4 v[226:227], v160, 1.0 op_sel:[1,1,0]
	v_pk_fma_f32 v[60:61], v[226:227], v[216:217], v[60:61] op_sel:[0,1,0] op_sel_hi:[1,1,1]
	v_cvt_scalef32_pk_f32_fp4 v[220:221], v161, 1.0
	v_pk_fma_f32 v[58:59], v[220:221], v[216:217], v[58:59] op_sel:[0,1,0] op_sel_hi:[1,1,1]
	v_cvt_scalef32_pk_f32_fp4 v[222:223], v161, 1.0 op_sel:[1,0,0]
	v_pk_fma_f32 v[56:57], v[222:223], v[216:217], v[56:57] op_sel:[0,1,0] op_sel_hi:[1,1,1]
	v_cvt_scalef32_pk_f32_fp4 v[224:225], v161, 1.0 op_sel:[0,1,0]
	v_pk_fma_f32 v[54:55], v[224:225], v[216:217], v[54:55] op_sel:[0,1,0] op_sel_hi:[1,1,1]
	v_cvt_scalef32_pk_f32_fp4 v[226:227], v161, 1.0 op_sel:[1,1,0]
	v_pk_fma_f32 v[52:53], v[226:227], v[216:217], v[52:53] op_sel:[0,1,0] op_sel_hi:[1,1,1]
	v_cvt_scalef32_pk_f32_fp4 v[220:221], v162, 1.0
	v_pk_fma_f32 v[50:51], v[220:221], v[216:217], v[50:51] op_sel:[0,1,0] op_sel_hi:[1,1,1]
	v_cvt_scalef32_pk_f32_fp4 v[222:223], v162, 1.0 op_sel:[1,0,0]
	v_pk_fma_f32 v[46:47], v[222:223], v[216:217], v[46:47] op_sel:[0,1,0] op_sel_hi:[1,1,1]
	v_cvt_scalef32_pk_f32_fp4 v[224:225], v162, 1.0 op_sel:[0,1,0]
	v_pk_fma_f32 v[44:45], v[224:225], v[216:217], v[44:45] op_sel:[0,1,0] op_sel_hi:[1,1,1]
	v_cvt_scalef32_pk_f32_fp4 v[226:227], v162, 1.0 op_sel:[1,1,0]
	v_pk_fma_f32 v[42:43], v[226:227], v[216:217], v[42:43] op_sel:[0,1,0] op_sel_hi:[1,1,1]
	v_cvt_scalef32_pk_f32_fp4 v[220:221], v163, 1.0
	v_pk_fma_f32 v[40:41], v[220:221], v[216:217], v[40:41] op_sel:[0,1,0] op_sel_hi:[1,1,1]
	v_cvt_scalef32_pk_f32_fp4 v[222:223], v163, 1.0 op_sel:[1,0,0]
	v_pk_fma_f32 v[38:39], v[222:223], v[216:217], v[38:39] op_sel:[0,1,0] op_sel_hi:[1,1,1]
	v_cvt_scalef32_pk_f32_fp4 v[224:225], v163, 1.0 op_sel:[0,1,0]
	v_pk_fma_f32 v[36:37], v[224:225], v[216:217], v[36:37] op_sel:[0,1,0] op_sel_hi:[1,1,1]
	v_cvt_scalef32_pk_f32_fp4 v[226:227], v163, 1.0 op_sel:[1,1,0]
	v_pk_fma_f32 v[34:35], v[226:227], v[216:217], v[34:35] op_sel:[0,1,0] op_sel_hi:[1,1,1]
	s_waitcnt vmcnt(10)
	v_cvt_scalef32_pk_f32_fp4 v[220:221], v164, 1.0
	v_pk_fma_f32 v[96:97], v[220:221], v[218:219], v[96:97] op_sel_hi:[1,0,1]
	v_cvt_scalef32_pk_f32_fp4 v[222:223], v164, 1.0 op_sel:[1,0,0]
	v_pk_fma_f32 v[98:99], v[222:223], v[218:219], v[98:99] op_sel_hi:[1,0,1]
	v_cvt_scalef32_pk_f32_fp4 v[224:225], v164, 1.0 op_sel:[0,1,0]
	v_pk_fma_f32 v[94:95], v[224:225], v[218:219], v[94:95] op_sel_hi:[1,0,1]
	v_cvt_scalef32_pk_f32_fp4 v[226:227], v164, 1.0 op_sel:[1,1,0]
	v_pk_fma_f32 v[92:93], v[226:227], v[218:219], v[92:93] op_sel_hi:[1,0,1]
	v_cvt_scalef32_pk_f32_fp4 v[220:221], v165, 1.0
	v_pk_fma_f32 v[90:91], v[220:221], v[218:219], v[90:91] op_sel_hi:[1,0,1]
	v_cvt_scalef32_pk_f32_fp4 v[222:223], v165, 1.0 op_sel:[1,0,0]
	v_pk_fma_f32 v[88:89], v[222:223], v[218:219], v[88:89] op_sel_hi:[1,0,1]
	v_cvt_scalef32_pk_f32_fp4 v[224:225], v165, 1.0 op_sel:[0,1,0]
	v_pk_fma_f32 v[86:87], v[224:225], v[218:219], v[86:87] op_sel_hi:[1,0,1]
	v_cvt_scalef32_pk_f32_fp4 v[226:227], v165, 1.0 op_sel:[1,1,0]
	v_pk_fma_f32 v[84:85], v[226:227], v[218:219], v[84:85] op_sel_hi:[1,0,1]
	v_cvt_scalef32_pk_f32_fp4 v[220:221], v166, 1.0
	v_pk_fma_f32 v[82:83], v[220:221], v[218:219], v[82:83] op_sel_hi:[1,0,1]
	v_cvt_scalef32_pk_f32_fp4 v[222:223], v166, 1.0 op_sel:[1,0,0]
	v_pk_fma_f32 v[80:81], v[222:223], v[218:219], v[80:81] op_sel_hi:[1,0,1]
	v_cvt_scalef32_pk_f32_fp4 v[224:225], v166, 1.0 op_sel:[0,1,0]
	v_pk_fma_f32 v[78:79], v[224:225], v[218:219], v[78:79] op_sel_hi:[1,0,1]
	v_cvt_scalef32_pk_f32_fp4 v[226:227], v166, 1.0 op_sel:[1,1,0]
	v_pk_fma_f32 v[76:77], v[226:227], v[218:219], v[76:77] op_sel_hi:[1,0,1]
	v_cvt_scalef32_pk_f32_fp4 v[220:221], v167, 1.0
	v_pk_fma_f32 v[74:75], v[220:221], v[218:219], v[74:75] op_sel_hi:[1,0,1]
	v_cvt_scalef32_pk_f32_fp4 v[222:223], v167, 1.0 op_sel:[1,0,0]
	v_pk_fma_f32 v[72:73], v[222:223], v[218:219], v[72:73] op_sel_hi:[1,0,1]
	v_cvt_scalef32_pk_f32_fp4 v[224:225], v167, 1.0 op_sel:[0,1,0]
	v_pk_fma_f32 v[70:71], v[224:225], v[218:219], v[70:71] op_sel_hi:[1,0,1]
	v_cvt_scalef32_pk_f32_fp4 v[226:227], v167, 1.0 op_sel:[1,1,0]
	v_pk_fma_f32 v[68:69], v[226:227], v[218:219], v[68:69] op_sel_hi:[1,0,1]
	v_cvt_scalef32_pk_f32_fp4 v[220:221], v168, 1.0
	v_pk_fma_f32 v[66:67], v[220:221], v[218:219], v[66:67] op_sel_hi:[1,0,1]
	v_cvt_scalef32_pk_f32_fp4 v[222:223], v168, 1.0 op_sel:[1,0,0]
	v_pk_fma_f32 v[64:65], v[222:223], v[218:219], v[64:65] op_sel_hi:[1,0,1]
	v_cvt_scalef32_pk_f32_fp4 v[224:225], v168, 1.0 op_sel:[0,1,0]
	v_pk_fma_f32 v[62:63], v[224:225], v[218:219], v[62:63] op_sel_hi:[1,0,1]
	v_cvt_scalef32_pk_f32_fp4 v[226:227], v168, 1.0 op_sel:[1,1,0]
	v_pk_fma_f32 v[60:61], v[226:227], v[218:219], v[60:61] op_sel_hi:[1,0,1]
	v_cvt_scalef32_pk_f32_fp4 v[220:221], v169, 1.0
	v_pk_fma_f32 v[58:59], v[220:221], v[218:219], v[58:59] op_sel_hi:[1,0,1]
	v_cvt_scalef32_pk_f32_fp4 v[222:223], v169, 1.0 op_sel:[1,0,0]
	v_pk_fma_f32 v[56:57], v[222:223], v[218:219], v[56:57] op_sel_hi:[1,0,1]
	v_cvt_scalef32_pk_f32_fp4 v[224:225], v169, 1.0 op_sel:[0,1,0]
	v_pk_fma_f32 v[54:55], v[224:225], v[218:219], v[54:55] op_sel_hi:[1,0,1]
	v_cvt_scalef32_pk_f32_fp4 v[226:227], v169, 1.0 op_sel:[1,1,0]
	v_pk_fma_f32 v[52:53], v[226:227], v[218:219], v[52:53] op_sel_hi:[1,0,1]
	v_cvt_scalef32_pk_f32_fp4 v[220:221], v170, 1.0
	v_pk_fma_f32 v[50:51], v[220:221], v[218:219], v[50:51] op_sel_hi:[1,0,1]
	v_cvt_scalef32_pk_f32_fp4 v[222:223], v170, 1.0 op_sel:[1,0,0]
	v_pk_fma_f32 v[46:47], v[222:223], v[218:219], v[46:47] op_sel_hi:[1,0,1]
	v_cvt_scalef32_pk_f32_fp4 v[224:225], v170, 1.0 op_sel:[0,1,0]
	v_pk_fma_f32 v[44:45], v[224:225], v[218:219], v[44:45] op_sel_hi:[1,0,1]
	v_cvt_scalef32_pk_f32_fp4 v[226:227], v170, 1.0 op_sel:[1,1,0]
	v_pk_fma_f32 v[42:43], v[226:227], v[218:219], v[42:43] op_sel_hi:[1,0,1]
	v_cvt_scalef32_pk_f32_fp4 v[220:221], v171, 1.0
	v_pk_fma_f32 v[40:41], v[220:221], v[218:219], v[40:41] op_sel_hi:[1,0,1]
	v_cvt_scalef32_pk_f32_fp4 v[222:223], v171, 1.0 op_sel:[1,0,0]
	v_pk_fma_f32 v[38:39], v[222:223], v[218:219], v[38:39] op_sel_hi:[1,0,1]
	v_cvt_scalef32_pk_f32_fp4 v[224:225], v171, 1.0 op_sel:[0,1,0]
	v_pk_fma_f32 v[36:37], v[224:225], v[218:219], v[36:37] op_sel_hi:[1,0,1]
	v_cvt_scalef32_pk_f32_fp4 v[226:227], v171, 1.0 op_sel:[1,1,0]
	v_pk_fma_f32 v[34:35], v[226:227], v[218:219], v[34:35] op_sel_hi:[1,0,1]
	s_waitcnt vmcnt(8)
	v_cvt_scalef32_pk_f32_fp4 v[220:221], v172, 1.0
	v_pk_fma_f32 v[96:97], v[220:221], v[218:219], v[96:97] op_sel:[0,1,0] op_sel_hi:[1,1,1]
	v_cvt_scalef32_pk_f32_fp4 v[222:223], v172, 1.0 op_sel:[1,0,0]
	v_pk_fma_f32 v[98:99], v[222:223], v[218:219], v[98:99] op_sel:[0,1,0] op_sel_hi:[1,1,1]
	v_cvt_scalef32_pk_f32_fp4 v[224:225], v172, 1.0 op_sel:[0,1,0]
	v_pk_fma_f32 v[94:95], v[224:225], v[218:219], v[94:95] op_sel:[0,1,0] op_sel_hi:[1,1,1]
	v_cvt_scalef32_pk_f32_fp4 v[226:227], v172, 1.0 op_sel:[1,1,0]
	v_pk_fma_f32 v[92:93], v[226:227], v[218:219], v[92:93] op_sel:[0,1,0] op_sel_hi:[1,1,1]
	v_cvt_scalef32_pk_f32_fp4 v[220:221], v173, 1.0
	v_pk_fma_f32 v[90:91], v[220:221], v[218:219], v[90:91] op_sel:[0,1,0] op_sel_hi:[1,1,1]
	v_cvt_scalef32_pk_f32_fp4 v[222:223], v173, 1.0 op_sel:[1,0,0]
	v_pk_fma_f32 v[88:89], v[222:223], v[218:219], v[88:89] op_sel:[0,1,0] op_sel_hi:[1,1,1]
	v_cvt_scalef32_pk_f32_fp4 v[224:225], v173, 1.0 op_sel:[0,1,0]
	v_pk_fma_f32 v[86:87], v[224:225], v[218:219], v[86:87] op_sel:[0,1,0] op_sel_hi:[1,1,1]
	v_cvt_scalef32_pk_f32_fp4 v[226:227], v173, 1.0 op_sel:[1,1,0]
	v_pk_fma_f32 v[84:85], v[226:227], v[218:219], v[84:85] op_sel:[0,1,0] op_sel_hi:[1,1,1]
	v_cvt_scalef32_pk_f32_fp4 v[220:221], v174, 1.0
	v_pk_fma_f32 v[82:83], v[220:221], v[218:219], v[82:83] op_sel:[0,1,0] op_sel_hi:[1,1,1]
	v_cvt_scalef32_pk_f32_fp4 v[222:223], v174, 1.0 op_sel:[1,0,0]
	v_pk_fma_f32 v[80:81], v[222:223], v[218:219], v[80:81] op_sel:[0,1,0] op_sel_hi:[1,1,1]
	v_cvt_scalef32_pk_f32_fp4 v[224:225], v174, 1.0 op_sel:[0,1,0]
	v_pk_fma_f32 v[78:79], v[224:225], v[218:219], v[78:79] op_sel:[0,1,0] op_sel_hi:[1,1,1]
	v_cvt_scalef32_pk_f32_fp4 v[226:227], v174, 1.0 op_sel:[1,1,0]
	v_pk_fma_f32 v[76:77], v[226:227], v[218:219], v[76:77] op_sel:[0,1,0] op_sel_hi:[1,1,1]
	v_cvt_scalef32_pk_f32_fp4 v[220:221], v175, 1.0
	v_pk_fma_f32 v[74:75], v[220:221], v[218:219], v[74:75] op_sel:[0,1,0] op_sel_hi:[1,1,1]
	v_cvt_scalef32_pk_f32_fp4 v[222:223], v175, 1.0 op_sel:[1,0,0]
	v_pk_fma_f32 v[72:73], v[222:223], v[218:219], v[72:73] op_sel:[0,1,0] op_sel_hi:[1,1,1]
	v_cvt_scalef32_pk_f32_fp4 v[224:225], v175, 1.0 op_sel:[0,1,0]
	v_pk_fma_f32 v[70:71], v[224:225], v[218:219], v[70:71] op_sel:[0,1,0] op_sel_hi:[1,1,1]
	v_cvt_scalef32_pk_f32_fp4 v[226:227], v175, 1.0 op_sel:[1,1,0]
	v_pk_fma_f32 v[68:69], v[226:227], v[218:219], v[68:69] op_sel:[0,1,0] op_sel_hi:[1,1,1]
	v_cvt_scalef32_pk_f32_fp4 v[220:221], v176, 1.0
	v_pk_fma_f32 v[66:67], v[220:221], v[218:219], v[66:67] op_sel:[0,1,0] op_sel_hi:[1,1,1]
	v_cvt_scalef32_pk_f32_fp4 v[222:223], v176, 1.0 op_sel:[1,0,0]
	v_pk_fma_f32 v[64:65], v[222:223], v[218:219], v[64:65] op_sel:[0,1,0] op_sel_hi:[1,1,1]
	v_cvt_scalef32_pk_f32_fp4 v[224:225], v176, 1.0 op_sel:[0,1,0]
	v_pk_fma_f32 v[62:63], v[224:225], v[218:219], v[62:63] op_sel:[0,1,0] op_sel_hi:[1,1,1]
	v_cvt_scalef32_pk_f32_fp4 v[226:227], v176, 1.0 op_sel:[1,1,0]
	v_pk_fma_f32 v[60:61], v[226:227], v[218:219], v[60:61] op_sel:[0,1,0] op_sel_hi:[1,1,1]
	v_cvt_scalef32_pk_f32_fp4 v[220:221], v177, 1.0
	v_pk_fma_f32 v[58:59], v[220:221], v[218:219], v[58:59] op_sel:[0,1,0] op_sel_hi:[1,1,1]
	v_cvt_scalef32_pk_f32_fp4 v[222:223], v177, 1.0 op_sel:[1,0,0]
	v_pk_fma_f32 v[56:57], v[222:223], v[218:219], v[56:57] op_sel:[0,1,0] op_sel_hi:[1,1,1]
	v_cvt_scalef32_pk_f32_fp4 v[224:225], v177, 1.0 op_sel:[0,1,0]
	v_pk_fma_f32 v[54:55], v[224:225], v[218:219], v[54:55] op_sel:[0,1,0] op_sel_hi:[1,1,1]
	v_cvt_scalef32_pk_f32_fp4 v[226:227], v177, 1.0 op_sel:[1,1,0]
	v_pk_fma_f32 v[52:53], v[226:227], v[218:219], v[52:53] op_sel:[0,1,0] op_sel_hi:[1,1,1]
	v_cvt_scalef32_pk_f32_fp4 v[220:221], v178, 1.0
	v_pk_fma_f32 v[50:51], v[220:221], v[218:219], v[50:51] op_sel:[0,1,0] op_sel_hi:[1,1,1]
	v_cvt_scalef32_pk_f32_fp4 v[222:223], v178, 1.0 op_sel:[1,0,0]
	v_pk_fma_f32 v[46:47], v[222:223], v[218:219], v[46:47] op_sel:[0,1,0] op_sel_hi:[1,1,1]
	v_cvt_scalef32_pk_f32_fp4 v[224:225], v178, 1.0 op_sel:[0,1,0]
	v_pk_fma_f32 v[44:45], v[224:225], v[218:219], v[44:45] op_sel:[0,1,0] op_sel_hi:[1,1,1]
	v_cvt_scalef32_pk_f32_fp4 v[226:227], v178, 1.0 op_sel:[1,1,0]
	v_pk_fma_f32 v[42:43], v[226:227], v[218:219], v[42:43] op_sel:[0,1,0] op_sel_hi:[1,1,1]
	v_cvt_scalef32_pk_f32_fp4 v[220:221], v179, 1.0
	v_pk_fma_f32 v[40:41], v[220:221], v[218:219], v[40:41] op_sel:[0,1,0] op_sel_hi:[1,1,1]
	v_cvt_scalef32_pk_f32_fp4 v[222:223], v179, 1.0 op_sel:[1,0,0]
	v_pk_fma_f32 v[38:39], v[222:223], v[218:219], v[38:39] op_sel:[0,1,0] op_sel_hi:[1,1,1]
	v_cvt_scalef32_pk_f32_fp4 v[224:225], v179, 1.0 op_sel:[0,1,0]
	v_pk_fma_f32 v[36:37], v[224:225], v[218:219], v[36:37] op_sel:[0,1,0] op_sel_hi:[1,1,1]
	v_cvt_scalef32_pk_f32_fp4 v[226:227], v179, 1.0 op_sel:[1,1,0]
	v_pk_fma_f32 v[34:35], v[226:227], v[218:219], v[34:35] op_sel:[0,1,0] op_sel_hi:[1,1,1]
	v_readfirstlane_b32 s60, v212
	v_readfirstlane_b32 s61, v213
	v_readfirstlane_b32 s62, v214
	v_readfirstlane_b32 s63, v215
	s_lshl_b32 s60, s60, 11
	v_add_u32_e32 v101, s60, v100
	global_load_dwordx4 v[148:151], v101, s[58:59]
	global_load_dwordx4 v[152:155], v101, s[58:59] offset:1024
	s_lshl_b32 s61, s61, 11
	v_add_u32_e32 v101, s61, v100
	global_load_dwordx4 v[156:159], v101, s[58:59]
	global_load_dwordx4 v[160:163], v101, s[58:59] offset:1024
	s_lshl_b32 s62, s62, 11
	v_add_u32_e32 v101, s62, v100
	global_load_dwordx4 v[164:167], v101, s[58:59]
	global_load_dwordx4 v[168:171], v101, s[58:59] offset:1024
	s_lshl_b32 s63, s63, 11
	v_add_u32_e32 v101, s63, v100
	global_load_dwordx4 v[172:175], v101, s[58:59]
	global_load_dwordx4 v[176:179], v101, s[58:59] offset:1024
	ds_read_b128 v[212:215], v102 offset:48
	ds_read_b128 v[216:219], v102 offset:528
	s_waitcnt lgkmcnt(0)
	s_waitcnt vmcnt(14)
	v_cvt_scalef32_pk_f32_fp4 v[220:221], v180, 1.0
	v_pk_fma_f32 v[96:97], v[220:221], v[216:217], v[96:97] op_sel_hi:[1,0,1]
	v_cvt_scalef32_pk_f32_fp4 v[222:223], v180, 1.0 op_sel:[1,0,0]
	v_pk_fma_f32 v[98:99], v[222:223], v[216:217], v[98:99] op_sel_hi:[1,0,1]
	v_cvt_scalef32_pk_f32_fp4 v[224:225], v180, 1.0 op_sel:[0,1,0]
	v_pk_fma_f32 v[94:95], v[224:225], v[216:217], v[94:95] op_sel_hi:[1,0,1]
	v_cvt_scalef32_pk_f32_fp4 v[226:227], v180, 1.0 op_sel:[1,1,0]
	v_pk_fma_f32 v[92:93], v[226:227], v[216:217], v[92:93] op_sel_hi:[1,0,1]
	v_cvt_scalef32_pk_f32_fp4 v[220:221], v181, 1.0
	v_pk_fma_f32 v[90:91], v[220:221], v[216:217], v[90:91] op_sel_hi:[1,0,1]
	v_cvt_scalef32_pk_f32_fp4 v[222:223], v181, 1.0 op_sel:[1,0,0]
	v_pk_fma_f32 v[88:89], v[222:223], v[216:217], v[88:89] op_sel_hi:[1,0,1]
	v_cvt_scalef32_pk_f32_fp4 v[224:225], v181, 1.0 op_sel:[0,1,0]
	v_pk_fma_f32 v[86:87], v[224:225], v[216:217], v[86:87] op_sel_hi:[1,0,1]
	v_cvt_scalef32_pk_f32_fp4 v[226:227], v181, 1.0 op_sel:[1,1,0]
	v_pk_fma_f32 v[84:85], v[226:227], v[216:217], v[84:85] op_sel_hi:[1,0,1]
	v_cvt_scalef32_pk_f32_fp4 v[220:221], v182, 1.0
	v_pk_fma_f32 v[82:83], v[220:221], v[216:217], v[82:83] op_sel_hi:[1,0,1]
	v_cvt_scalef32_pk_f32_fp4 v[222:223], v182, 1.0 op_sel:[1,0,0]
	v_pk_fma_f32 v[80:81], v[222:223], v[216:217], v[80:81] op_sel_hi:[1,0,1]
	v_cvt_scalef32_pk_f32_fp4 v[224:225], v182, 1.0 op_sel:[0,1,0]
	v_pk_fma_f32 v[78:79], v[224:225], v[216:217], v[78:79] op_sel_hi:[1,0,1]
	v_cvt_scalef32_pk_f32_fp4 v[226:227], v182, 1.0 op_sel:[1,1,0]
	v_pk_fma_f32 v[76:77], v[226:227], v[216:217], v[76:77] op_sel_hi:[1,0,1]
	v_cvt_scalef32_pk_f32_fp4 v[220:221], v183, 1.0
	v_pk_fma_f32 v[74:75], v[220:221], v[216:217], v[74:75] op_sel_hi:[1,0,1]
	v_cvt_scalef32_pk_f32_fp4 v[222:223], v183, 1.0 op_sel:[1,0,0]
	v_pk_fma_f32 v[72:73], v[222:223], v[216:217], v[72:73] op_sel_hi:[1,0,1]
	v_cvt_scalef32_pk_f32_fp4 v[224:225], v183, 1.0 op_sel:[0,1,0]
	v_pk_fma_f32 v[70:71], v[224:225], v[216:217], v[70:71] op_sel_hi:[1,0,1]
	v_cvt_scalef32_pk_f32_fp4 v[226:227], v183, 1.0 op_sel:[1,1,0]
	v_pk_fma_f32 v[68:69], v[226:227], v[216:217], v[68:69] op_sel_hi:[1,0,1]
	v_cvt_scalef32_pk_f32_fp4 v[220:221], v184, 1.0
	v_pk_fma_f32 v[66:67], v[220:221], v[216:217], v[66:67] op_sel_hi:[1,0,1]
	v_cvt_scalef32_pk_f32_fp4 v[222:223], v184, 1.0 op_sel:[1,0,0]
	v_pk_fma_f32 v[64:65], v[222:223], v[216:217], v[64:65] op_sel_hi:[1,0,1]
	v_cvt_scalef32_pk_f32_fp4 v[224:225], v184, 1.0 op_sel:[0,1,0]
	v_pk_fma_f32 v[62:63], v[224:225], v[216:217], v[62:63] op_sel_hi:[1,0,1]
	v_cvt_scalef32_pk_f32_fp4 v[226:227], v184, 1.0 op_sel:[1,1,0]
	v_pk_fma_f32 v[60:61], v[226:227], v[216:217], v[60:61] op_sel_hi:[1,0,1]
	v_cvt_scalef32_pk_f32_fp4 v[220:221], v185, 1.0
	v_pk_fma_f32 v[58:59], v[220:221], v[216:217], v[58:59] op_sel_hi:[1,0,1]
	v_cvt_scalef32_pk_f32_fp4 v[222:223], v185, 1.0 op_sel:[1,0,0]
	v_pk_fma_f32 v[56:57], v[222:223], v[216:217], v[56:57] op_sel_hi:[1,0,1]
	v_cvt_scalef32_pk_f32_fp4 v[224:225], v185, 1.0 op_sel:[0,1,0]
	v_pk_fma_f32 v[54:55], v[224:225], v[216:217], v[54:55] op_sel_hi:[1,0,1]
	v_cvt_scalef32_pk_f32_fp4 v[226:227], v185, 1.0 op_sel:[1,1,0]
	v_pk_fma_f32 v[52:53], v[226:227], v[216:217], v[52:53] op_sel_hi:[1,0,1]
	v_cvt_scalef32_pk_f32_fp4 v[220:221], v186, 1.0
	v_pk_fma_f32 v[50:51], v[220:221], v[216:217], v[50:51] op_sel_hi:[1,0,1]
	v_cvt_scalef32_pk_f32_fp4 v[222:223], v186, 1.0 op_sel:[1,0,0]
	v_pk_fma_f32 v[46:47], v[222:223], v[216:217], v[46:47] op_sel_hi:[1,0,1]
	v_cvt_scalef32_pk_f32_fp4 v[224:225], v186, 1.0 op_sel:[0,1,0]
	v_pk_fma_f32 v[44:45], v[224:225], v[216:217], v[44:45] op_sel_hi:[1,0,1]
	v_cvt_scalef32_pk_f32_fp4 v[226:227], v186, 1.0 op_sel:[1,1,0]
	v_pk_fma_f32 v[42:43], v[226:227], v[216:217], v[42:43] op_sel_hi:[1,0,1]
	v_cvt_scalef32_pk_f32_fp4 v[220:221], v187, 1.0
	v_pk_fma_f32 v[40:41], v[220:221], v[216:217], v[40:41] op_sel_hi:[1,0,1]
	v_cvt_scalef32_pk_f32_fp4 v[222:223], v187, 1.0 op_sel:[1,0,0]
	v_pk_fma_f32 v[38:39], v[222:223], v[216:217], v[38:39] op_sel_hi:[1,0,1]
	v_cvt_scalef32_pk_f32_fp4 v[224:225], v187, 1.0 op_sel:[0,1,0]
	v_pk_fma_f32 v[36:37], v[224:225], v[216:217], v[36:37] op_sel_hi:[1,0,1]
	v_cvt_scalef32_pk_f32_fp4 v[226:227], v187, 1.0 op_sel:[1,1,0]
	v_pk_fma_f32 v[34:35], v[226:227], v[216:217], v[34:35] op_sel_hi:[1,0,1]
	s_waitcnt vmcnt(12)
	v_cvt_scalef32_pk_f32_fp4 v[220:221], v188, 1.0
	v_pk_fma_f32 v[96:97], v[220:221], v[216:217], v[96:97] op_sel:[0,1,0] op_sel_hi:[1,1,1]
	v_cvt_scalef32_pk_f32_fp4 v[222:223], v188, 1.0 op_sel:[1,0,0]
	v_pk_fma_f32 v[98:99], v[222:223], v[216:217], v[98:99] op_sel:[0,1,0] op_sel_hi:[1,1,1]
	v_cvt_scalef32_pk_f32_fp4 v[224:225], v188, 1.0 op_sel:[0,1,0]
	v_pk_fma_f32 v[94:95], v[224:225], v[216:217], v[94:95] op_sel:[0,1,0] op_sel_hi:[1,1,1]
	v_cvt_scalef32_pk_f32_fp4 v[226:227], v188, 1.0 op_sel:[1,1,0]
	v_pk_fma_f32 v[92:93], v[226:227], v[216:217], v[92:93] op_sel:[0,1,0] op_sel_hi:[1,1,1]
	v_cvt_scalef32_pk_f32_fp4 v[220:221], v189, 1.0
	v_pk_fma_f32 v[90:91], v[220:221], v[216:217], v[90:91] op_sel:[0,1,0] op_sel_hi:[1,1,1]
	v_cvt_scalef32_pk_f32_fp4 v[222:223], v189, 1.0 op_sel:[1,0,0]
	v_pk_fma_f32 v[88:89], v[222:223], v[216:217], v[88:89] op_sel:[0,1,0] op_sel_hi:[1,1,1]
	v_cvt_scalef32_pk_f32_fp4 v[224:225], v189, 1.0 op_sel:[0,1,0]
	v_pk_fma_f32 v[86:87], v[224:225], v[216:217], v[86:87] op_sel:[0,1,0] op_sel_hi:[1,1,1]
	v_cvt_scalef32_pk_f32_fp4 v[226:227], v189, 1.0 op_sel:[1,1,0]
	v_pk_fma_f32 v[84:85], v[226:227], v[216:217], v[84:85] op_sel:[0,1,0] op_sel_hi:[1,1,1]
	v_cvt_scalef32_pk_f32_fp4 v[220:221], v190, 1.0
	v_pk_fma_f32 v[82:83], v[220:221], v[216:217], v[82:83] op_sel:[0,1,0] op_sel_hi:[1,1,1]
	v_cvt_scalef32_pk_f32_fp4 v[222:223], v190, 1.0 op_sel:[1,0,0]
	v_pk_fma_f32 v[80:81], v[222:223], v[216:217], v[80:81] op_sel:[0,1,0] op_sel_hi:[1,1,1]
	v_cvt_scalef32_pk_f32_fp4 v[224:225], v190, 1.0 op_sel:[0,1,0]
	v_pk_fma_f32 v[78:79], v[224:225], v[216:217], v[78:79] op_sel:[0,1,0] op_sel_hi:[1,1,1]
	v_cvt_scalef32_pk_f32_fp4 v[226:227], v190, 1.0 op_sel:[1,1,0]
	v_pk_fma_f32 v[76:77], v[226:227], v[216:217], v[76:77] op_sel:[0,1,0] op_sel_hi:[1,1,1]
	v_cvt_scalef32_pk_f32_fp4 v[220:221], v191, 1.0
	v_pk_fma_f32 v[74:75], v[220:221], v[216:217], v[74:75] op_sel:[0,1,0] op_sel_hi:[1,1,1]
	v_cvt_scalef32_pk_f32_fp4 v[222:223], v191, 1.0 op_sel:[1,0,0]
	v_pk_fma_f32 v[72:73], v[222:223], v[216:217], v[72:73] op_sel:[0,1,0] op_sel_hi:[1,1,1]
	v_cvt_scalef32_pk_f32_fp4 v[224:225], v191, 1.0 op_sel:[0,1,0]
	v_pk_fma_f32 v[70:71], v[224:225], v[216:217], v[70:71] op_sel:[0,1,0] op_sel_hi:[1,1,1]
	v_cvt_scalef32_pk_f32_fp4 v[226:227], v191, 1.0 op_sel:[1,1,0]
	v_pk_fma_f32 v[68:69], v[226:227], v[216:217], v[68:69] op_sel:[0,1,0] op_sel_hi:[1,1,1]
	v_cvt_scalef32_pk_f32_fp4 v[220:221], v192, 1.0
	v_pk_fma_f32 v[66:67], v[220:221], v[216:217], v[66:67] op_sel:[0,1,0] op_sel_hi:[1,1,1]
	v_cvt_scalef32_pk_f32_fp4 v[222:223], v192, 1.0 op_sel:[1,0,0]
	v_pk_fma_f32 v[64:65], v[222:223], v[216:217], v[64:65] op_sel:[0,1,0] op_sel_hi:[1,1,1]
	v_cvt_scalef32_pk_f32_fp4 v[224:225], v192, 1.0 op_sel:[0,1,0]
	v_pk_fma_f32 v[62:63], v[224:225], v[216:217], v[62:63] op_sel:[0,1,0] op_sel_hi:[1,1,1]
	v_cvt_scalef32_pk_f32_fp4 v[226:227], v192, 1.0 op_sel:[1,1,0]
	v_pk_fma_f32 v[60:61], v[226:227], v[216:217], v[60:61] op_sel:[0,1,0] op_sel_hi:[1,1,1]
	v_cvt_scalef32_pk_f32_fp4 v[220:221], v193, 1.0
	v_pk_fma_f32 v[58:59], v[220:221], v[216:217], v[58:59] op_sel:[0,1,0] op_sel_hi:[1,1,1]
	v_cvt_scalef32_pk_f32_fp4 v[222:223], v193, 1.0 op_sel:[1,0,0]
	v_pk_fma_f32 v[56:57], v[222:223], v[216:217], v[56:57] op_sel:[0,1,0] op_sel_hi:[1,1,1]
	v_cvt_scalef32_pk_f32_fp4 v[224:225], v193, 1.0 op_sel:[0,1,0]
	v_pk_fma_f32 v[54:55], v[224:225], v[216:217], v[54:55] op_sel:[0,1,0] op_sel_hi:[1,1,1]
	v_cvt_scalef32_pk_f32_fp4 v[226:227], v193, 1.0 op_sel:[1,1,0]
	v_pk_fma_f32 v[52:53], v[226:227], v[216:217], v[52:53] op_sel:[0,1,0] op_sel_hi:[1,1,1]
	v_cvt_scalef32_pk_f32_fp4 v[220:221], v194, 1.0
	v_pk_fma_f32 v[50:51], v[220:221], v[216:217], v[50:51] op_sel:[0,1,0] op_sel_hi:[1,1,1]
	v_cvt_scalef32_pk_f32_fp4 v[222:223], v194, 1.0 op_sel:[1,0,0]
	v_pk_fma_f32 v[46:47], v[222:223], v[216:217], v[46:47] op_sel:[0,1,0] op_sel_hi:[1,1,1]
	v_cvt_scalef32_pk_f32_fp4 v[224:225], v194, 1.0 op_sel:[0,1,0]
	v_pk_fma_f32 v[44:45], v[224:225], v[216:217], v[44:45] op_sel:[0,1,0] op_sel_hi:[1,1,1]
	v_cvt_scalef32_pk_f32_fp4 v[226:227], v194, 1.0 op_sel:[1,1,0]
	v_pk_fma_f32 v[42:43], v[226:227], v[216:217], v[42:43] op_sel:[0,1,0] op_sel_hi:[1,1,1]
	v_cvt_scalef32_pk_f32_fp4 v[220:221], v195, 1.0
	v_pk_fma_f32 v[40:41], v[220:221], v[216:217], v[40:41] op_sel:[0,1,0] op_sel_hi:[1,1,1]
	v_cvt_scalef32_pk_f32_fp4 v[222:223], v195, 1.0 op_sel:[1,0,0]
	v_pk_fma_f32 v[38:39], v[222:223], v[216:217], v[38:39] op_sel:[0,1,0] op_sel_hi:[1,1,1]
	v_cvt_scalef32_pk_f32_fp4 v[224:225], v195, 1.0 op_sel:[0,1,0]
	v_pk_fma_f32 v[36:37], v[224:225], v[216:217], v[36:37] op_sel:[0,1,0] op_sel_hi:[1,1,1]
	v_cvt_scalef32_pk_f32_fp4 v[226:227], v195, 1.0 op_sel:[1,1,0]
	v_pk_fma_f32 v[34:35], v[226:227], v[216:217], v[34:35] op_sel:[0,1,0] op_sel_hi:[1,1,1]
	s_waitcnt vmcnt(10)
	v_cvt_scalef32_pk_f32_fp4 v[220:221], v196, 1.0
	v_pk_fma_f32 v[96:97], v[220:221], v[218:219], v[96:97] op_sel_hi:[1,0,1]
	v_cvt_scalef32_pk_f32_fp4 v[222:223], v196, 1.0 op_sel:[1,0,0]
	v_pk_fma_f32 v[98:99], v[222:223], v[218:219], v[98:99] op_sel_hi:[1,0,1]
	v_cvt_scalef32_pk_f32_fp4 v[224:225], v196, 1.0 op_sel:[0,1,0]
	v_pk_fma_f32 v[94:95], v[224:225], v[218:219], v[94:95] op_sel_hi:[1,0,1]
	v_cvt_scalef32_pk_f32_fp4 v[226:227], v196, 1.0 op_sel:[1,1,0]
	v_pk_fma_f32 v[92:93], v[226:227], v[218:219], v[92:93] op_sel_hi:[1,0,1]
	v_cvt_scalef32_pk_f32_fp4 v[220:221], v197, 1.0
	v_pk_fma_f32 v[90:91], v[220:221], v[218:219], v[90:91] op_sel_hi:[1,0,1]
	v_cvt_scalef32_pk_f32_fp4 v[222:223], v197, 1.0 op_sel:[1,0,0]
	v_pk_fma_f32 v[88:89], v[222:223], v[218:219], v[88:89] op_sel_hi:[1,0,1]
	v_cvt_scalef32_pk_f32_fp4 v[224:225], v197, 1.0 op_sel:[0,1,0]
	v_pk_fma_f32 v[86:87], v[224:225], v[218:219], v[86:87] op_sel_hi:[1,0,1]
	v_cvt_scalef32_pk_f32_fp4 v[226:227], v197, 1.0 op_sel:[1,1,0]
	v_pk_fma_f32 v[84:85], v[226:227], v[218:219], v[84:85] op_sel_hi:[1,0,1]
	v_cvt_scalef32_pk_f32_fp4 v[220:221], v198, 1.0
	v_pk_fma_f32 v[82:83], v[220:221], v[218:219], v[82:83] op_sel_hi:[1,0,1]
	v_cvt_scalef32_pk_f32_fp4 v[222:223], v198, 1.0 op_sel:[1,0,0]
	v_pk_fma_f32 v[80:81], v[222:223], v[218:219], v[80:81] op_sel_hi:[1,0,1]
	v_cvt_scalef32_pk_f32_fp4 v[224:225], v198, 1.0 op_sel:[0,1,0]
	v_pk_fma_f32 v[78:79], v[224:225], v[218:219], v[78:79] op_sel_hi:[1,0,1]
	v_cvt_scalef32_pk_f32_fp4 v[226:227], v198, 1.0 op_sel:[1,1,0]
	v_pk_fma_f32 v[76:77], v[226:227], v[218:219], v[76:77] op_sel_hi:[1,0,1]
	v_cvt_scalef32_pk_f32_fp4 v[220:221], v199, 1.0
	v_pk_fma_f32 v[74:75], v[220:221], v[218:219], v[74:75] op_sel_hi:[1,0,1]
	v_cvt_scalef32_pk_f32_fp4 v[222:223], v199, 1.0 op_sel:[1,0,0]
	v_pk_fma_f32 v[72:73], v[222:223], v[218:219], v[72:73] op_sel_hi:[1,0,1]
	v_cvt_scalef32_pk_f32_fp4 v[224:225], v199, 1.0 op_sel:[0,1,0]
	v_pk_fma_f32 v[70:71], v[224:225], v[218:219], v[70:71] op_sel_hi:[1,0,1]
	v_cvt_scalef32_pk_f32_fp4 v[226:227], v199, 1.0 op_sel:[1,1,0]
	v_pk_fma_f32 v[68:69], v[226:227], v[218:219], v[68:69] op_sel_hi:[1,0,1]
	v_cvt_scalef32_pk_f32_fp4 v[220:221], v200, 1.0
	v_pk_fma_f32 v[66:67], v[220:221], v[218:219], v[66:67] op_sel_hi:[1,0,1]
	v_cvt_scalef32_pk_f32_fp4 v[222:223], v200, 1.0 op_sel:[1,0,0]
	v_pk_fma_f32 v[64:65], v[222:223], v[218:219], v[64:65] op_sel_hi:[1,0,1]
	v_cvt_scalef32_pk_f32_fp4 v[224:225], v200, 1.0 op_sel:[0,1,0]
	v_pk_fma_f32 v[62:63], v[224:225], v[218:219], v[62:63] op_sel_hi:[1,0,1]
	v_cvt_scalef32_pk_f32_fp4 v[226:227], v200, 1.0 op_sel:[1,1,0]
	v_pk_fma_f32 v[60:61], v[226:227], v[218:219], v[60:61] op_sel_hi:[1,0,1]
	v_cvt_scalef32_pk_f32_fp4 v[220:221], v201, 1.0
	v_pk_fma_f32 v[58:59], v[220:221], v[218:219], v[58:59] op_sel_hi:[1,0,1]
	v_cvt_scalef32_pk_f32_fp4 v[222:223], v201, 1.0 op_sel:[1,0,0]
	v_pk_fma_f32 v[56:57], v[222:223], v[218:219], v[56:57] op_sel_hi:[1,0,1]
	v_cvt_scalef32_pk_f32_fp4 v[224:225], v201, 1.0 op_sel:[0,1,0]
	v_pk_fma_f32 v[54:55], v[224:225], v[218:219], v[54:55] op_sel_hi:[1,0,1]
	v_cvt_scalef32_pk_f32_fp4 v[226:227], v201, 1.0 op_sel:[1,1,0]
	v_pk_fma_f32 v[52:53], v[226:227], v[218:219], v[52:53] op_sel_hi:[1,0,1]
	v_cvt_scalef32_pk_f32_fp4 v[220:221], v202, 1.0
	v_pk_fma_f32 v[50:51], v[220:221], v[218:219], v[50:51] op_sel_hi:[1,0,1]
	v_cvt_scalef32_pk_f32_fp4 v[222:223], v202, 1.0 op_sel:[1,0,0]
	v_pk_fma_f32 v[46:47], v[222:223], v[218:219], v[46:47] op_sel_hi:[1,0,1]
	v_cvt_scalef32_pk_f32_fp4 v[224:225], v202, 1.0 op_sel:[0,1,0]
	v_pk_fma_f32 v[44:45], v[224:225], v[218:219], v[44:45] op_sel_hi:[1,0,1]
	v_cvt_scalef32_pk_f32_fp4 v[226:227], v202, 1.0 op_sel:[1,1,0]
	v_pk_fma_f32 v[42:43], v[226:227], v[218:219], v[42:43] op_sel_hi:[1,0,1]
	v_cvt_scalef32_pk_f32_fp4 v[220:221], v203, 1.0
	v_pk_fma_f32 v[40:41], v[220:221], v[218:219], v[40:41] op_sel_hi:[1,0,1]
	v_cvt_scalef32_pk_f32_fp4 v[222:223], v203, 1.0 op_sel:[1,0,0]
	v_pk_fma_f32 v[38:39], v[222:223], v[218:219], v[38:39] op_sel_hi:[1,0,1]
	v_cvt_scalef32_pk_f32_fp4 v[224:225], v203, 1.0 op_sel:[0,1,0]
	v_pk_fma_f32 v[36:37], v[224:225], v[218:219], v[36:37] op_sel_hi:[1,0,1]
	v_cvt_scalef32_pk_f32_fp4 v[226:227], v203, 1.0 op_sel:[1,1,0]
	v_pk_fma_f32 v[34:35], v[226:227], v[218:219], v[34:35] op_sel_hi:[1,0,1]
	s_waitcnt vmcnt(8)
	v_cvt_scalef32_pk_f32_fp4 v[220:221], v204, 1.0
	v_pk_fma_f32 v[96:97], v[220:221], v[218:219], v[96:97] op_sel:[0,1,0] op_sel_hi:[1,1,1]
	v_cvt_scalef32_pk_f32_fp4 v[222:223], v204, 1.0 op_sel:[1,0,0]
	v_pk_fma_f32 v[98:99], v[222:223], v[218:219], v[98:99] op_sel:[0,1,0] op_sel_hi:[1,1,1]
	v_cvt_scalef32_pk_f32_fp4 v[224:225], v204, 1.0 op_sel:[0,1,0]
	v_pk_fma_f32 v[94:95], v[224:225], v[218:219], v[94:95] op_sel:[0,1,0] op_sel_hi:[1,1,1]
	v_cvt_scalef32_pk_f32_fp4 v[226:227], v204, 1.0 op_sel:[1,1,0]
	v_pk_fma_f32 v[92:93], v[226:227], v[218:219], v[92:93] op_sel:[0,1,0] op_sel_hi:[1,1,1]
	v_cvt_scalef32_pk_f32_fp4 v[220:221], v205, 1.0
	v_pk_fma_f32 v[90:91], v[220:221], v[218:219], v[90:91] op_sel:[0,1,0] op_sel_hi:[1,1,1]
	v_cvt_scalef32_pk_f32_fp4 v[222:223], v205, 1.0 op_sel:[1,0,0]
	v_pk_fma_f32 v[88:89], v[222:223], v[218:219], v[88:89] op_sel:[0,1,0] op_sel_hi:[1,1,1]
	v_cvt_scalef32_pk_f32_fp4 v[224:225], v205, 1.0 op_sel:[0,1,0]
	v_pk_fma_f32 v[86:87], v[224:225], v[218:219], v[86:87] op_sel:[0,1,0] op_sel_hi:[1,1,1]
	v_cvt_scalef32_pk_f32_fp4 v[226:227], v205, 1.0 op_sel:[1,1,0]
	v_pk_fma_f32 v[84:85], v[226:227], v[218:219], v[84:85] op_sel:[0,1,0] op_sel_hi:[1,1,1]
	v_cvt_scalef32_pk_f32_fp4 v[220:221], v206, 1.0
	v_pk_fma_f32 v[82:83], v[220:221], v[218:219], v[82:83] op_sel:[0,1,0] op_sel_hi:[1,1,1]
	v_cvt_scalef32_pk_f32_fp4 v[222:223], v206, 1.0 op_sel:[1,0,0]
	v_pk_fma_f32 v[80:81], v[222:223], v[218:219], v[80:81] op_sel:[0,1,0] op_sel_hi:[1,1,1]
	v_cvt_scalef32_pk_f32_fp4 v[224:225], v206, 1.0 op_sel:[0,1,0]
	v_pk_fma_f32 v[78:79], v[224:225], v[218:219], v[78:79] op_sel:[0,1,0] op_sel_hi:[1,1,1]
	v_cvt_scalef32_pk_f32_fp4 v[226:227], v206, 1.0 op_sel:[1,1,0]
	v_pk_fma_f32 v[76:77], v[226:227], v[218:219], v[76:77] op_sel:[0,1,0] op_sel_hi:[1,1,1]
	v_cvt_scalef32_pk_f32_fp4 v[220:221], v207, 1.0
	v_pk_fma_f32 v[74:75], v[220:221], v[218:219], v[74:75] op_sel:[0,1,0] op_sel_hi:[1,1,1]
	v_cvt_scalef32_pk_f32_fp4 v[222:223], v207, 1.0 op_sel:[1,0,0]
	v_pk_fma_f32 v[72:73], v[222:223], v[218:219], v[72:73] op_sel:[0,1,0] op_sel_hi:[1,1,1]
	v_cvt_scalef32_pk_f32_fp4 v[224:225], v207, 1.0 op_sel:[0,1,0]
	v_pk_fma_f32 v[70:71], v[224:225], v[218:219], v[70:71] op_sel:[0,1,0] op_sel_hi:[1,1,1]
	v_cvt_scalef32_pk_f32_fp4 v[226:227], v207, 1.0 op_sel:[1,1,0]
	v_pk_fma_f32 v[68:69], v[226:227], v[218:219], v[68:69] op_sel:[0,1,0] op_sel_hi:[1,1,1]
	v_cvt_scalef32_pk_f32_fp4 v[220:221], v208, 1.0
	v_pk_fma_f32 v[66:67], v[220:221], v[218:219], v[66:67] op_sel:[0,1,0] op_sel_hi:[1,1,1]
	v_cvt_scalef32_pk_f32_fp4 v[222:223], v208, 1.0 op_sel:[1,0,0]
	v_pk_fma_f32 v[64:65], v[222:223], v[218:219], v[64:65] op_sel:[0,1,0] op_sel_hi:[1,1,1]
	v_cvt_scalef32_pk_f32_fp4 v[224:225], v208, 1.0 op_sel:[0,1,0]
	v_pk_fma_f32 v[62:63], v[224:225], v[218:219], v[62:63] op_sel:[0,1,0] op_sel_hi:[1,1,1]
	v_cvt_scalef32_pk_f32_fp4 v[226:227], v208, 1.0 op_sel:[1,1,0]
	v_pk_fma_f32 v[60:61], v[226:227], v[218:219], v[60:61] op_sel:[0,1,0] op_sel_hi:[1,1,1]
	v_cvt_scalef32_pk_f32_fp4 v[220:221], v209, 1.0
	v_pk_fma_f32 v[58:59], v[220:221], v[218:219], v[58:59] op_sel:[0,1,0] op_sel_hi:[1,1,1]
	v_cvt_scalef32_pk_f32_fp4 v[222:223], v209, 1.0 op_sel:[1,0,0]
	v_pk_fma_f32 v[56:57], v[222:223], v[218:219], v[56:57] op_sel:[0,1,0] op_sel_hi:[1,1,1]
	v_cvt_scalef32_pk_f32_fp4 v[224:225], v209, 1.0 op_sel:[0,1,0]
	v_pk_fma_f32 v[54:55], v[224:225], v[218:219], v[54:55] op_sel:[0,1,0] op_sel_hi:[1,1,1]
	v_cvt_scalef32_pk_f32_fp4 v[226:227], v209, 1.0 op_sel:[1,1,0]
	v_pk_fma_f32 v[52:53], v[226:227], v[218:219], v[52:53] op_sel:[0,1,0] op_sel_hi:[1,1,1]
	v_cvt_scalef32_pk_f32_fp4 v[220:221], v210, 1.0
	v_pk_fma_f32 v[50:51], v[220:221], v[218:219], v[50:51] op_sel:[0,1,0] op_sel_hi:[1,1,1]
	v_cvt_scalef32_pk_f32_fp4 v[222:223], v210, 1.0 op_sel:[1,0,0]
	v_pk_fma_f32 v[46:47], v[222:223], v[218:219], v[46:47] op_sel:[0,1,0] op_sel_hi:[1,1,1]
	v_cvt_scalef32_pk_f32_fp4 v[224:225], v210, 1.0 op_sel:[0,1,0]
	v_pk_fma_f32 v[44:45], v[224:225], v[218:219], v[44:45] op_sel:[0,1,0] op_sel_hi:[1,1,1]
	v_cvt_scalef32_pk_f32_fp4 v[226:227], v210, 1.0 op_sel:[1,1,0]
	v_pk_fma_f32 v[42:43], v[226:227], v[218:219], v[42:43] op_sel:[0,1,0] op_sel_hi:[1,1,1]
	v_cvt_scalef32_pk_f32_fp4 v[220:221], v211, 1.0
	v_pk_fma_f32 v[40:41], v[220:221], v[218:219], v[40:41] op_sel:[0,1,0] op_sel_hi:[1,1,1]
	v_cvt_scalef32_pk_f32_fp4 v[222:223], v211, 1.0 op_sel:[1,0,0]
	v_pk_fma_f32 v[38:39], v[222:223], v[218:219], v[38:39] op_sel:[0,1,0] op_sel_hi:[1,1,1]
	v_cvt_scalef32_pk_f32_fp4 v[224:225], v211, 1.0 op_sel:[0,1,0]
	v_pk_fma_f32 v[36:37], v[224:225], v[218:219], v[36:37] op_sel:[0,1,0] op_sel_hi:[1,1,1]
	v_cvt_scalef32_pk_f32_fp4 v[226:227], v211, 1.0 op_sel:[1,1,0]
	v_pk_fma_f32 v[34:35], v[226:227], v[218:219], v[34:35] op_sel:[0,1,0] op_sel_hi:[1,1,1]
	v_readfirstlane_b32 s60, v212
	v_readfirstlane_b32 s61, v213
	v_readfirstlane_b32 s62, v214
	v_readfirstlane_b32 s63, v215
	s_lshl_b32 s60, s60, 11
	v_add_u32_e32 v101, s60, v100
	global_load_dwordx4 v[180:183], v101, s[58:59]
	global_load_dwordx4 v[184:187], v101, s[58:59] offset:1024
	s_lshl_b32 s61, s61, 11
	v_add_u32_e32 v101, s61, v100
	global_load_dwordx4 v[188:191], v101, s[58:59]
	global_load_dwordx4 v[192:195], v101, s[58:59] offset:1024
	s_lshl_b32 s62, s62, 11
	v_add_u32_e32 v101, s62, v100
	global_load_dwordx4 v[196:199], v101, s[58:59]
	global_load_dwordx4 v[200:203], v101, s[58:59] offset:1024
	s_lshl_b32 s63, s63, 11
	v_add_u32_e32 v101, s63, v100
	global_load_dwordx4 v[204:207], v101, s[58:59]
	global_load_dwordx4 v[208:211], v101, s[58:59] offset:1024
	v_add_u32_e32 v102, 32, v102
	s_add_u32 s10, s10, 1
	s_cmp_lt_u32 s10, 15
	s_cbranch_scc1 .Lpv_loop
	ds_read_b128 v[216:219], v102 offset:512
	s_waitcnt lgkmcnt(0)
	s_waitcnt vmcnt(14)
	v_cvt_scalef32_pk_f32_fp4 v[220:221], v148, 1.0
	v_pk_fma_f32 v[96:97], v[220:221], v[216:217], v[96:97] op_sel_hi:[1,0,1]
	v_cvt_scalef32_pk_f32_fp4 v[222:223], v148, 1.0 op_sel:[1,0,0]
	v_pk_fma_f32 v[98:99], v[222:223], v[216:217], v[98:99] op_sel_hi:[1,0,1]
	v_cvt_scalef32_pk_f32_fp4 v[224:225], v148, 1.0 op_sel:[0,1,0]
	v_pk_fma_f32 v[94:95], v[224:225], v[216:217], v[94:95] op_sel_hi:[1,0,1]
	v_cvt_scalef32_pk_f32_fp4 v[226:227], v148, 1.0 op_sel:[1,1,0]
	v_pk_fma_f32 v[92:93], v[226:227], v[216:217], v[92:93] op_sel_hi:[1,0,1]
	v_cvt_scalef32_pk_f32_fp4 v[220:221], v149, 1.0
	v_pk_fma_f32 v[90:91], v[220:221], v[216:217], v[90:91] op_sel_hi:[1,0,1]
	v_cvt_scalef32_pk_f32_fp4 v[222:223], v149, 1.0 op_sel:[1,0,0]
	v_pk_fma_f32 v[88:89], v[222:223], v[216:217], v[88:89] op_sel_hi:[1,0,1]
	v_cvt_scalef32_pk_f32_fp4 v[224:225], v149, 1.0 op_sel:[0,1,0]
	v_pk_fma_f32 v[86:87], v[224:225], v[216:217], v[86:87] op_sel_hi:[1,0,1]
	v_cvt_scalef32_pk_f32_fp4 v[226:227], v149, 1.0 op_sel:[1,1,0]
	v_pk_fma_f32 v[84:85], v[226:227], v[216:217], v[84:85] op_sel_hi:[1,0,1]
	v_cvt_scalef32_pk_f32_fp4 v[220:221], v150, 1.0
	v_pk_fma_f32 v[82:83], v[220:221], v[216:217], v[82:83] op_sel_hi:[1,0,1]
	v_cvt_scalef32_pk_f32_fp4 v[222:223], v150, 1.0 op_sel:[1,0,0]
	v_pk_fma_f32 v[80:81], v[222:223], v[216:217], v[80:81] op_sel_hi:[1,0,1]
	v_cvt_scalef32_pk_f32_fp4 v[224:225], v150, 1.0 op_sel:[0,1,0]
	v_pk_fma_f32 v[78:79], v[224:225], v[216:217], v[78:79] op_sel_hi:[1,0,1]
	v_cvt_scalef32_pk_f32_fp4 v[226:227], v150, 1.0 op_sel:[1,1,0]
	v_pk_fma_f32 v[76:77], v[226:227], v[216:217], v[76:77] op_sel_hi:[1,0,1]
	v_cvt_scalef32_pk_f32_fp4 v[220:221], v151, 1.0
	v_pk_fma_f32 v[74:75], v[220:221], v[216:217], v[74:75] op_sel_hi:[1,0,1]
	v_cvt_scalef32_pk_f32_fp4 v[222:223], v151, 1.0 op_sel:[1,0,0]
	v_pk_fma_f32 v[72:73], v[222:223], v[216:217], v[72:73] op_sel_hi:[1,0,1]
	v_cvt_scalef32_pk_f32_fp4 v[224:225], v151, 1.0 op_sel:[0,1,0]
	v_pk_fma_f32 v[70:71], v[224:225], v[216:217], v[70:71] op_sel_hi:[1,0,1]
	v_cvt_scalef32_pk_f32_fp4 v[226:227], v151, 1.0 op_sel:[1,1,0]
	v_pk_fma_f32 v[68:69], v[226:227], v[216:217], v[68:69] op_sel_hi:[1,0,1]
	v_cvt_scalef32_pk_f32_fp4 v[220:221], v152, 1.0
	v_pk_fma_f32 v[66:67], v[220:221], v[216:217], v[66:67] op_sel_hi:[1,0,1]
	v_cvt_scalef32_pk_f32_fp4 v[222:223], v152, 1.0 op_sel:[1,0,0]
	v_pk_fma_f32 v[64:65], v[222:223], v[216:217], v[64:65] op_sel_hi:[1,0,1]
	v_cvt_scalef32_pk_f32_fp4 v[224:225], v152, 1.0 op_sel:[0,1,0]
	v_pk_fma_f32 v[62:63], v[224:225], v[216:217], v[62:63] op_sel_hi:[1,0,1]
	v_cvt_scalef32_pk_f32_fp4 v[226:227], v152, 1.0 op_sel:[1,1,0]
	v_pk_fma_f32 v[60:61], v[226:227], v[216:217], v[60:61] op_sel_hi:[1,0,1]
	v_cvt_scalef32_pk_f32_fp4 v[220:221], v153, 1.0
	v_pk_fma_f32 v[58:59], v[220:221], v[216:217], v[58:59] op_sel_hi:[1,0,1]
	v_cvt_scalef32_pk_f32_fp4 v[222:223], v153, 1.0 op_sel:[1,0,0]
	v_pk_fma_f32 v[56:57], v[222:223], v[216:217], v[56:57] op_sel_hi:[1,0,1]
	v_cvt_scalef32_pk_f32_fp4 v[224:225], v153, 1.0 op_sel:[0,1,0]
	v_pk_fma_f32 v[54:55], v[224:225], v[216:217], v[54:55] op_sel_hi:[1,0,1]
	v_cvt_scalef32_pk_f32_fp4 v[226:227], v153, 1.0 op_sel:[1,1,0]
	v_pk_fma_f32 v[52:53], v[226:227], v[216:217], v[52:53] op_sel_hi:[1,0,1]
	v_cvt_scalef32_pk_f32_fp4 v[220:221], v154, 1.0
	v_pk_fma_f32 v[50:51], v[220:221], v[216:217], v[50:51] op_sel_hi:[1,0,1]
	v_cvt_scalef32_pk_f32_fp4 v[222:223], v154, 1.0 op_sel:[1,0,0]
	v_pk_fma_f32 v[46:47], v[222:223], v[216:217], v[46:47] op_sel_hi:[1,0,1]
	v_cvt_scalef32_pk_f32_fp4 v[224:225], v154, 1.0 op_sel:[0,1,0]
	v_pk_fma_f32 v[44:45], v[224:225], v[216:217], v[44:45] op_sel_hi:[1,0,1]
	v_cvt_scalef32_pk_f32_fp4 v[226:227], v154, 1.0 op_sel:[1,1,0]
	v_pk_fma_f32 v[42:43], v[226:227], v[216:217], v[42:43] op_sel_hi:[1,0,1]
	v_cvt_scalef32_pk_f32_fp4 v[220:221], v155, 1.0
	v_pk_fma_f32 v[40:41], v[220:221], v[216:217], v[40:41] op_sel_hi:[1,0,1]
	v_cvt_scalef32_pk_f32_fp4 v[222:223], v155, 1.0 op_sel:[1,0,0]
	v_pk_fma_f32 v[38:39], v[222:223], v[216:217], v[38:39] op_sel_hi:[1,0,1]
	v_cvt_scalef32_pk_f32_fp4 v[224:225], v155, 1.0 op_sel:[0,1,0]
	v_pk_fma_f32 v[36:37], v[224:225], v[216:217], v[36:37] op_sel_hi:[1,0,1]
	v_cvt_scalef32_pk_f32_fp4 v[226:227], v155, 1.0 op_sel:[1,1,0]
	v_pk_fma_f32 v[34:35], v[226:227], v[216:217], v[34:35] op_sel_hi:[1,0,1]
	s_waitcnt vmcnt(12)
	v_cvt_scalef32_pk_f32_fp4 v[220:221], v156, 1.0
	v_pk_fma_f32 v[96:97], v[220:221], v[216:217], v[96:97] op_sel:[0,1,0] op_sel_hi:[1,1,1]
	v_cvt_scalef32_pk_f32_fp4 v[222:223], v156, 1.0 op_sel:[1,0,0]
	v_pk_fma_f32 v[98:99], v[222:223], v[216:217], v[98:99] op_sel:[0,1,0] op_sel_hi:[1,1,1]
	v_cvt_scalef32_pk_f32_fp4 v[224:225], v156, 1.0 op_sel:[0,1,0]
	v_pk_fma_f32 v[94:95], v[224:225], v[216:217], v[94:95] op_sel:[0,1,0] op_sel_hi:[1,1,1]
	v_cvt_scalef32_pk_f32_fp4 v[226:227], v156, 1.0 op_sel:[1,1,0]
	v_pk_fma_f32 v[92:93], v[226:227], v[216:217], v[92:93] op_sel:[0,1,0] op_sel_hi:[1,1,1]
	v_cvt_scalef32_pk_f32_fp4 v[220:221], v157, 1.0
	v_pk_fma_f32 v[90:91], v[220:221], v[216:217], v[90:91] op_sel:[0,1,0] op_sel_hi:[1,1,1]
	v_cvt_scalef32_pk_f32_fp4 v[222:223], v157, 1.0 op_sel:[1,0,0]
	v_pk_fma_f32 v[88:89], v[222:223], v[216:217], v[88:89] op_sel:[0,1,0] op_sel_hi:[1,1,1]
	v_cvt_scalef32_pk_f32_fp4 v[224:225], v157, 1.0 op_sel:[0,1,0]
	v_pk_fma_f32 v[86:87], v[224:225], v[216:217], v[86:87] op_sel:[0,1,0] op_sel_hi:[1,1,1]
	v_cvt_scalef32_pk_f32_fp4 v[226:227], v157, 1.0 op_sel:[1,1,0]
	v_pk_fma_f32 v[84:85], v[226:227], v[216:217], v[84:85] op_sel:[0,1,0] op_sel_hi:[1,1,1]
	v_cvt_scalef32_pk_f32_fp4 v[220:221], v158, 1.0
	v_pk_fma_f32 v[82:83], v[220:221], v[216:217], v[82:83] op_sel:[0,1,0] op_sel_hi:[1,1,1]
	v_cvt_scalef32_pk_f32_fp4 v[222:223], v158, 1.0 op_sel:[1,0,0]
	v_pk_fma_f32 v[80:81], v[222:223], v[216:217], v[80:81] op_sel:[0,1,0] op_sel_hi:[1,1,1]
	v_cvt_scalef32_pk_f32_fp4 v[224:225], v158, 1.0 op_sel:[0,1,0]
	v_pk_fma_f32 v[78:79], v[224:225], v[216:217], v[78:79] op_sel:[0,1,0] op_sel_hi:[1,1,1]
	v_cvt_scalef32_pk_f32_fp4 v[226:227], v158, 1.0 op_sel:[1,1,0]
	v_pk_fma_f32 v[76:77], v[226:227], v[216:217], v[76:77] op_sel:[0,1,0] op_sel_hi:[1,1,1]
	v_cvt_scalef32_pk_f32_fp4 v[220:221], v159, 1.0
	v_pk_fma_f32 v[74:75], v[220:221], v[216:217], v[74:75] op_sel:[0,1,0] op_sel_hi:[1,1,1]
	v_cvt_scalef32_pk_f32_fp4 v[222:223], v159, 1.0 op_sel:[1,0,0]
	v_pk_fma_f32 v[72:73], v[222:223], v[216:217], v[72:73] op_sel:[0,1,0] op_sel_hi:[1,1,1]
	v_cvt_scalef32_pk_f32_fp4 v[224:225], v159, 1.0 op_sel:[0,1,0]
	v_pk_fma_f32 v[70:71], v[224:225], v[216:217], v[70:71] op_sel:[0,1,0] op_sel_hi:[1,1,1]
	v_cvt_scalef32_pk_f32_fp4 v[226:227], v159, 1.0 op_sel:[1,1,0]
	v_pk_fma_f32 v[68:69], v[226:227], v[216:217], v[68:69] op_sel:[0,1,0] op_sel_hi:[1,1,1]
	v_cvt_scalef32_pk_f32_fp4 v[220:221], v160, 1.0
	v_pk_fma_f32 v[66:67], v[220:221], v[216:217], v[66:67] op_sel:[0,1,0] op_sel_hi:[1,1,1]
	v_cvt_scalef32_pk_f32_fp4 v[222:223], v160, 1.0 op_sel:[1,0,0]
	v_pk_fma_f32 v[64:65], v[222:223], v[216:217], v[64:65] op_sel:[0,1,0] op_sel_hi:[1,1,1]
	v_cvt_scalef32_pk_f32_fp4 v[224:225], v160, 1.0 op_sel:[0,1,0]
	v_pk_fma_f32 v[62:63], v[224:225], v[216:217], v[62:63] op_sel:[0,1,0] op_sel_hi:[1,1,1]
	v_cvt_scalef32_pk_f32_fp4 v[226:227], v160, 1.0 op_sel:[1,1,0]
	v_pk_fma_f32 v[60:61], v[226:227], v[216:217], v[60:61] op_sel:[0,1,0] op_sel_hi:[1,1,1]
	v_cvt_scalef32_pk_f32_fp4 v[220:221], v161, 1.0
	v_pk_fma_f32 v[58:59], v[220:221], v[216:217], v[58:59] op_sel:[0,1,0] op_sel_hi:[1,1,1]
	v_cvt_scalef32_pk_f32_fp4 v[222:223], v161, 1.0 op_sel:[1,0,0]
	v_pk_fma_f32 v[56:57], v[222:223], v[216:217], v[56:57] op_sel:[0,1,0] op_sel_hi:[1,1,1]
	v_cvt_scalef32_pk_f32_fp4 v[224:225], v161, 1.0 op_sel:[0,1,0]
	v_pk_fma_f32 v[54:55], v[224:225], v[216:217], v[54:55] op_sel:[0,1,0] op_sel_hi:[1,1,1]
	v_cvt_scalef32_pk_f32_fp4 v[226:227], v161, 1.0 op_sel:[1,1,0]
	v_pk_fma_f32 v[52:53], v[226:227], v[216:217], v[52:53] op_sel:[0,1,0] op_sel_hi:[1,1,1]
	v_cvt_scalef32_pk_f32_fp4 v[220:221], v162, 1.0
	v_pk_fma_f32 v[50:51], v[220:221], v[216:217], v[50:51] op_sel:[0,1,0] op_sel_hi:[1,1,1]
	v_cvt_scalef32_pk_f32_fp4 v[222:223], v162, 1.0 op_sel:[1,0,0]
	v_pk_fma_f32 v[46:47], v[222:223], v[216:217], v[46:47] op_sel:[0,1,0] op_sel_hi:[1,1,1]
	v_cvt_scalef32_pk_f32_fp4 v[224:225], v162, 1.0 op_sel:[0,1,0]
	v_pk_fma_f32 v[44:45], v[224:225], v[216:217], v[44:45] op_sel:[0,1,0] op_sel_hi:[1,1,1]
	v_cvt_scalef32_pk_f32_fp4 v[226:227], v162, 1.0 op_sel:[1,1,0]
	v_pk_fma_f32 v[42:43], v[226:227], v[216:217], v[42:43] op_sel:[0,1,0] op_sel_hi:[1,1,1]
	v_cvt_scalef32_pk_f32_fp4 v[220:221], v163, 1.0
	v_pk_fma_f32 v[40:41], v[220:221], v[216:217], v[40:41] op_sel:[0,1,0] op_sel_hi:[1,1,1]
	v_cvt_scalef32_pk_f32_fp4 v[222:223], v163, 1.0 op_sel:[1,0,0]
	v_pk_fma_f32 v[38:39], v[222:223], v[216:217], v[38:39] op_sel:[0,1,0] op_sel_hi:[1,1,1]
	v_cvt_scalef32_pk_f32_fp4 v[224:225], v163, 1.0 op_sel:[0,1,0]
	v_pk_fma_f32 v[36:37], v[224:225], v[216:217], v[36:37] op_sel:[0,1,0] op_sel_hi:[1,1,1]
	v_cvt_scalef32_pk_f32_fp4 v[226:227], v163, 1.0 op_sel:[1,1,0]
	v_pk_fma_f32 v[34:35], v[226:227], v[216:217], v[34:35] op_sel:[0,1,0] op_sel_hi:[1,1,1]
	s_waitcnt vmcnt(10)
	v_cvt_scalef32_pk_f32_fp4 v[220:221], v164, 1.0
	v_pk_fma_f32 v[96:97], v[220:221], v[218:219], v[96:97] op_sel_hi:[1,0,1]
	v_cvt_scalef32_pk_f32_fp4 v[222:223], v164, 1.0 op_sel:[1,0,0]
	v_pk_fma_f32 v[98:99], v[222:223], v[218:219], v[98:99] op_sel_hi:[1,0,1]
	v_cvt_scalef32_pk_f32_fp4 v[224:225], v164, 1.0 op_sel:[0,1,0]
	v_pk_fma_f32 v[94:95], v[224:225], v[218:219], v[94:95] op_sel_hi:[1,0,1]
	v_cvt_scalef32_pk_f32_fp4 v[226:227], v164, 1.0 op_sel:[1,1,0]
	v_pk_fma_f32 v[92:93], v[226:227], v[218:219], v[92:93] op_sel_hi:[1,0,1]
	v_cvt_scalef32_pk_f32_fp4 v[220:221], v165, 1.0
	v_pk_fma_f32 v[90:91], v[220:221], v[218:219], v[90:91] op_sel_hi:[1,0,1]
	v_cvt_scalef32_pk_f32_fp4 v[222:223], v165, 1.0 op_sel:[1,0,0]
	v_pk_fma_f32 v[88:89], v[222:223], v[218:219], v[88:89] op_sel_hi:[1,0,1]
	v_cvt_scalef32_pk_f32_fp4 v[224:225], v165, 1.0 op_sel:[0,1,0]
	v_pk_fma_f32 v[86:87], v[224:225], v[218:219], v[86:87] op_sel_hi:[1,0,1]
	v_cvt_scalef32_pk_f32_fp4 v[226:227], v165, 1.0 op_sel:[1,1,0]
	v_pk_fma_f32 v[84:85], v[226:227], v[218:219], v[84:85] op_sel_hi:[1,0,1]
	v_cvt_scalef32_pk_f32_fp4 v[220:221], v166, 1.0
	v_pk_fma_f32 v[82:83], v[220:221], v[218:219], v[82:83] op_sel_hi:[1,0,1]
	v_cvt_scalef32_pk_f32_fp4 v[222:223], v166, 1.0 op_sel:[1,0,0]
	v_pk_fma_f32 v[80:81], v[222:223], v[218:219], v[80:81] op_sel_hi:[1,0,1]
	v_cvt_scalef32_pk_f32_fp4 v[224:225], v166, 1.0 op_sel:[0,1,0]
	v_pk_fma_f32 v[78:79], v[224:225], v[218:219], v[78:79] op_sel_hi:[1,0,1]
	v_cvt_scalef32_pk_f32_fp4 v[226:227], v166, 1.0 op_sel:[1,1,0]
	v_pk_fma_f32 v[76:77], v[226:227], v[218:219], v[76:77] op_sel_hi:[1,0,1]
	v_cvt_scalef32_pk_f32_fp4 v[220:221], v167, 1.0
	v_pk_fma_f32 v[74:75], v[220:221], v[218:219], v[74:75] op_sel_hi:[1,0,1]
	v_cvt_scalef32_pk_f32_fp4 v[222:223], v167, 1.0 op_sel:[1,0,0]
	v_pk_fma_f32 v[72:73], v[222:223], v[218:219], v[72:73] op_sel_hi:[1,0,1]
	v_cvt_scalef32_pk_f32_fp4 v[224:225], v167, 1.0 op_sel:[0,1,0]
	v_pk_fma_f32 v[70:71], v[224:225], v[218:219], v[70:71] op_sel_hi:[1,0,1]
	v_cvt_scalef32_pk_f32_fp4 v[226:227], v167, 1.0 op_sel:[1,1,0]
	v_pk_fma_f32 v[68:69], v[226:227], v[218:219], v[68:69] op_sel_hi:[1,0,1]
	v_cvt_scalef32_pk_f32_fp4 v[220:221], v168, 1.0
	v_pk_fma_f32 v[66:67], v[220:221], v[218:219], v[66:67] op_sel_hi:[1,0,1]
	v_cvt_scalef32_pk_f32_fp4 v[222:223], v168, 1.0 op_sel:[1,0,0]
	v_pk_fma_f32 v[64:65], v[222:223], v[218:219], v[64:65] op_sel_hi:[1,0,1]
	v_cvt_scalef32_pk_f32_fp4 v[224:225], v168, 1.0 op_sel:[0,1,0]
	v_pk_fma_f32 v[62:63], v[224:225], v[218:219], v[62:63] op_sel_hi:[1,0,1]
	v_cvt_scalef32_pk_f32_fp4 v[226:227], v168, 1.0 op_sel:[1,1,0]
	v_pk_fma_f32 v[60:61], v[226:227], v[218:219], v[60:61] op_sel_hi:[1,0,1]
	v_cvt_scalef32_pk_f32_fp4 v[220:221], v169, 1.0
	v_pk_fma_f32 v[58:59], v[220:221], v[218:219], v[58:59] op_sel_hi:[1,0,1]
	v_cvt_scalef32_pk_f32_fp4 v[222:223], v169, 1.0 op_sel:[1,0,0]
	v_pk_fma_f32 v[56:57], v[222:223], v[218:219], v[56:57] op_sel_hi:[1,0,1]
	v_cvt_scalef32_pk_f32_fp4 v[224:225], v169, 1.0 op_sel:[0,1,0]
	v_pk_fma_f32 v[54:55], v[224:225], v[218:219], v[54:55] op_sel_hi:[1,0,1]
	v_cvt_scalef32_pk_f32_fp4 v[226:227], v169, 1.0 op_sel:[1,1,0]
	v_pk_fma_f32 v[52:53], v[226:227], v[218:219], v[52:53] op_sel_hi:[1,0,1]
	v_cvt_scalef32_pk_f32_fp4 v[220:221], v170, 1.0
	v_pk_fma_f32 v[50:51], v[220:221], v[218:219], v[50:51] op_sel_hi:[1,0,1]
	v_cvt_scalef32_pk_f32_fp4 v[222:223], v170, 1.0 op_sel:[1,0,0]
	v_pk_fma_f32 v[46:47], v[222:223], v[218:219], v[46:47] op_sel_hi:[1,0,1]
	v_cvt_scalef32_pk_f32_fp4 v[224:225], v170, 1.0 op_sel:[0,1,0]
	v_pk_fma_f32 v[44:45], v[224:225], v[218:219], v[44:45] op_sel_hi:[1,0,1]
	v_cvt_scalef32_pk_f32_fp4 v[226:227], v170, 1.0 op_sel:[1,1,0]
	v_pk_fma_f32 v[42:43], v[226:227], v[218:219], v[42:43] op_sel_hi:[1,0,1]
	v_cvt_scalef32_pk_f32_fp4 v[220:221], v171, 1.0
	v_pk_fma_f32 v[40:41], v[220:221], v[218:219], v[40:41] op_sel_hi:[1,0,1]
	v_cvt_scalef32_pk_f32_fp4 v[222:223], v171, 1.0 op_sel:[1,0,0]
	v_pk_fma_f32 v[38:39], v[222:223], v[218:219], v[38:39] op_sel_hi:[1,0,1]
	v_cvt_scalef32_pk_f32_fp4 v[224:225], v171, 1.0 op_sel:[0,1,0]
	v_pk_fma_f32 v[36:37], v[224:225], v[218:219], v[36:37] op_sel_hi:[1,0,1]
	v_cvt_scalef32_pk_f32_fp4 v[226:227], v171, 1.0 op_sel:[1,1,0]
	v_pk_fma_f32 v[34:35], v[226:227], v[218:219], v[34:35] op_sel_hi:[1,0,1]
	s_waitcnt vmcnt(8)
	v_cvt_scalef32_pk_f32_fp4 v[220:221], v172, 1.0
	v_pk_fma_f32 v[96:97], v[220:221], v[218:219], v[96:97] op_sel:[0,1,0] op_sel_hi:[1,1,1]
	v_cvt_scalef32_pk_f32_fp4 v[222:223], v172, 1.0 op_sel:[1,0,0]
	v_pk_fma_f32 v[98:99], v[222:223], v[218:219], v[98:99] op_sel:[0,1,0] op_sel_hi:[1,1,1]
	v_cvt_scalef32_pk_f32_fp4 v[224:225], v172, 1.0 op_sel:[0,1,0]
	v_pk_fma_f32 v[94:95], v[224:225], v[218:219], v[94:95] op_sel:[0,1,0] op_sel_hi:[1,1,1]
	v_cvt_scalef32_pk_f32_fp4 v[226:227], v172, 1.0 op_sel:[1,1,0]
	v_pk_fma_f32 v[92:93], v[226:227], v[218:219], v[92:93] op_sel:[0,1,0] op_sel_hi:[1,1,1]
	v_cvt_scalef32_pk_f32_fp4 v[220:221], v173, 1.0
	v_pk_fma_f32 v[90:91], v[220:221], v[218:219], v[90:91] op_sel:[0,1,0] op_sel_hi:[1,1,1]
	v_cvt_scalef32_pk_f32_fp4 v[222:223], v173, 1.0 op_sel:[1,0,0]
	v_pk_fma_f32 v[88:89], v[222:223], v[218:219], v[88:89] op_sel:[0,1,0] op_sel_hi:[1,1,1]
	v_cvt_scalef32_pk_f32_fp4 v[224:225], v173, 1.0 op_sel:[0,1,0]
	v_pk_fma_f32 v[86:87], v[224:225], v[218:219], v[86:87] op_sel:[0,1,0] op_sel_hi:[1,1,1]
	v_cvt_scalef32_pk_f32_fp4 v[226:227], v173, 1.0 op_sel:[1,1,0]
	v_pk_fma_f32 v[84:85], v[226:227], v[218:219], v[84:85] op_sel:[0,1,0] op_sel_hi:[1,1,1]
	v_cvt_scalef32_pk_f32_fp4 v[220:221], v174, 1.0
	v_pk_fma_f32 v[82:83], v[220:221], v[218:219], v[82:83] op_sel:[0,1,0] op_sel_hi:[1,1,1]
	v_cvt_scalef32_pk_f32_fp4 v[222:223], v174, 1.0 op_sel:[1,0,0]
	v_pk_fma_f32 v[80:81], v[222:223], v[218:219], v[80:81] op_sel:[0,1,0] op_sel_hi:[1,1,1]
	v_cvt_scalef32_pk_f32_fp4 v[224:225], v174, 1.0 op_sel:[0,1,0]
	v_pk_fma_f32 v[78:79], v[224:225], v[218:219], v[78:79] op_sel:[0,1,0] op_sel_hi:[1,1,1]
	v_cvt_scalef32_pk_f32_fp4 v[226:227], v174, 1.0 op_sel:[1,1,0]
	v_pk_fma_f32 v[76:77], v[226:227], v[218:219], v[76:77] op_sel:[0,1,0] op_sel_hi:[1,1,1]
	v_cvt_scalef32_pk_f32_fp4 v[220:221], v175, 1.0
	v_pk_fma_f32 v[74:75], v[220:221], v[218:219], v[74:75] op_sel:[0,1,0] op_sel_hi:[1,1,1]
	v_cvt_scalef32_pk_f32_fp4 v[222:223], v175, 1.0 op_sel:[1,0,0]
	v_pk_fma_f32 v[72:73], v[222:223], v[218:219], v[72:73] op_sel:[0,1,0] op_sel_hi:[1,1,1]
	v_cvt_scalef32_pk_f32_fp4 v[224:225], v175, 1.0 op_sel:[0,1,0]
	v_pk_fma_f32 v[70:71], v[224:225], v[218:219], v[70:71] op_sel:[0,1,0] op_sel_hi:[1,1,1]
	v_cvt_scalef32_pk_f32_fp4 v[226:227], v175, 1.0 op_sel:[1,1,0]
	v_pk_fma_f32 v[68:69], v[226:227], v[218:219], v[68:69] op_sel:[0,1,0] op_sel_hi:[1,1,1]
	v_cvt_scalef32_pk_f32_fp4 v[220:221], v176, 1.0
	v_pk_fma_f32 v[66:67], v[220:221], v[218:219], v[66:67] op_sel:[0,1,0] op_sel_hi:[1,1,1]
	v_cvt_scalef32_pk_f32_fp4 v[222:223], v176, 1.0 op_sel:[1,0,0]
	v_pk_fma_f32 v[64:65], v[222:223], v[218:219], v[64:65] op_sel:[0,1,0] op_sel_hi:[1,1,1]
	v_cvt_scalef32_pk_f32_fp4 v[224:225], v176, 1.0 op_sel:[0,1,0]
	v_pk_fma_f32 v[62:63], v[224:225], v[218:219], v[62:63] op_sel:[0,1,0] op_sel_hi:[1,1,1]
	v_cvt_scalef32_pk_f32_fp4 v[226:227], v176, 1.0 op_sel:[1,1,0]
	v_pk_fma_f32 v[60:61], v[226:227], v[218:219], v[60:61] op_sel:[0,1,0] op_sel_hi:[1,1,1]
	v_cvt_scalef32_pk_f32_fp4 v[220:221], v177, 1.0
	v_pk_fma_f32 v[58:59], v[220:221], v[218:219], v[58:59] op_sel:[0,1,0] op_sel_hi:[1,1,1]
	v_cvt_scalef32_pk_f32_fp4 v[222:223], v177, 1.0 op_sel:[1,0,0]
	v_pk_fma_f32 v[56:57], v[222:223], v[218:219], v[56:57] op_sel:[0,1,0] op_sel_hi:[1,1,1]
	v_cvt_scalef32_pk_f32_fp4 v[224:225], v177, 1.0 op_sel:[0,1,0]
	v_pk_fma_f32 v[54:55], v[224:225], v[218:219], v[54:55] op_sel:[0,1,0] op_sel_hi:[1,1,1]
	v_cvt_scalef32_pk_f32_fp4 v[226:227], v177, 1.0 op_sel:[1,1,0]
	v_pk_fma_f32 v[52:53], v[226:227], v[218:219], v[52:53] op_sel:[0,1,0] op_sel_hi:[1,1,1]
	v_cvt_scalef32_pk_f32_fp4 v[220:221], v178, 1.0
	v_pk_fma_f32 v[50:51], v[220:221], v[218:219], v[50:51] op_sel:[0,1,0] op_sel_hi:[1,1,1]
	v_cvt_scalef32_pk_f32_fp4 v[222:223], v178, 1.0 op_sel:[1,0,0]
	v_pk_fma_f32 v[46:47], v[222:223], v[218:219], v[46:47] op_sel:[0,1,0] op_sel_hi:[1,1,1]
	v_cvt_scalef32_pk_f32_fp4 v[224:225], v178, 1.0 op_sel:[0,1,0]
	v_pk_fma_f32 v[44:45], v[224:225], v[218:219], v[44:45] op_sel:[0,1,0] op_sel_hi:[1,1,1]
	v_cvt_scalef32_pk_f32_fp4 v[226:227], v178, 1.0 op_sel:[1,1,0]
	v_pk_fma_f32 v[42:43], v[226:227], v[218:219], v[42:43] op_sel:[0,1,0] op_sel_hi:[1,1,1]
	v_cvt_scalef32_pk_f32_fp4 v[220:221], v179, 1.0
	v_pk_fma_f32 v[40:41], v[220:221], v[218:219], v[40:41] op_sel:[0,1,0] op_sel_hi:[1,1,1]
	v_cvt_scalef32_pk_f32_fp4 v[222:223], v179, 1.0 op_sel:[1,0,0]
	v_pk_fma_f32 v[38:39], v[222:223], v[218:219], v[38:39] op_sel:[0,1,0] op_sel_hi:[1,1,1]
	v_cvt_scalef32_pk_f32_fp4 v[224:225], v179, 1.0 op_sel:[0,1,0]
	v_pk_fma_f32 v[36:37], v[224:225], v[218:219], v[36:37] op_sel:[0,1,0] op_sel_hi:[1,1,1]
	v_cvt_scalef32_pk_f32_fp4 v[226:227], v179, 1.0 op_sel:[1,1,0]
	v_pk_fma_f32 v[34:35], v[226:227], v[218:219], v[34:35] op_sel:[0,1,0] op_sel_hi:[1,1,1]
	ds_read_b128 v[216:219], v102 offset:528
	s_waitcnt lgkmcnt(0)
	s_waitcnt vmcnt(6)
	v_cvt_scalef32_pk_f32_fp4 v[220:221], v180, 1.0
	v_pk_fma_f32 v[96:97], v[220:221], v[216:217], v[96:97] op_sel_hi:[1,0,1]
	v_cvt_scalef32_pk_f32_fp4 v[222:223], v180, 1.0 op_sel:[1,0,0]
	v_pk_fma_f32 v[98:99], v[222:223], v[216:217], v[98:99] op_sel_hi:[1,0,1]
	v_cvt_scalef32_pk_f32_fp4 v[224:225], v180, 1.0 op_sel:[0,1,0]
	v_pk_fma_f32 v[94:95], v[224:225], v[216:217], v[94:95] op_sel_hi:[1,0,1]
	v_cvt_scalef32_pk_f32_fp4 v[226:227], v180, 1.0 op_sel:[1,1,0]
	v_pk_fma_f32 v[92:93], v[226:227], v[216:217], v[92:93] op_sel_hi:[1,0,1]
	v_cvt_scalef32_pk_f32_fp4 v[220:221], v181, 1.0
	v_pk_fma_f32 v[90:91], v[220:221], v[216:217], v[90:91] op_sel_hi:[1,0,1]
	v_cvt_scalef32_pk_f32_fp4 v[222:223], v181, 1.0 op_sel:[1,0,0]
	v_pk_fma_f32 v[88:89], v[222:223], v[216:217], v[88:89] op_sel_hi:[1,0,1]
	v_cvt_scalef32_pk_f32_fp4 v[224:225], v181, 1.0 op_sel:[0,1,0]
	v_pk_fma_f32 v[86:87], v[224:225], v[216:217], v[86:87] op_sel_hi:[1,0,1]
	v_cvt_scalef32_pk_f32_fp4 v[226:227], v181, 1.0 op_sel:[1,1,0]
	v_pk_fma_f32 v[84:85], v[226:227], v[216:217], v[84:85] op_sel_hi:[1,0,1]
	v_cvt_scalef32_pk_f32_fp4 v[220:221], v182, 1.0
	v_pk_fma_f32 v[82:83], v[220:221], v[216:217], v[82:83] op_sel_hi:[1,0,1]
	v_cvt_scalef32_pk_f32_fp4 v[222:223], v182, 1.0 op_sel:[1,0,0]
	v_pk_fma_f32 v[80:81], v[222:223], v[216:217], v[80:81] op_sel_hi:[1,0,1]
	v_cvt_scalef32_pk_f32_fp4 v[224:225], v182, 1.0 op_sel:[0,1,0]
	v_pk_fma_f32 v[78:79], v[224:225], v[216:217], v[78:79] op_sel_hi:[1,0,1]
	v_cvt_scalef32_pk_f32_fp4 v[226:227], v182, 1.0 op_sel:[1,1,0]
	v_pk_fma_f32 v[76:77], v[226:227], v[216:217], v[76:77] op_sel_hi:[1,0,1]
	v_cvt_scalef32_pk_f32_fp4 v[220:221], v183, 1.0
	v_pk_fma_f32 v[74:75], v[220:221], v[216:217], v[74:75] op_sel_hi:[1,0,1]
	v_cvt_scalef32_pk_f32_fp4 v[222:223], v183, 1.0 op_sel:[1,0,0]
	v_pk_fma_f32 v[72:73], v[222:223], v[216:217], v[72:73] op_sel_hi:[1,0,1]
	v_cvt_scalef32_pk_f32_fp4 v[224:225], v183, 1.0 op_sel:[0,1,0]
	v_pk_fma_f32 v[70:71], v[224:225], v[216:217], v[70:71] op_sel_hi:[1,0,1]
	v_cvt_scalef32_pk_f32_fp4 v[226:227], v183, 1.0 op_sel:[1,1,0]
	v_pk_fma_f32 v[68:69], v[226:227], v[216:217], v[68:69] op_sel_hi:[1,0,1]
	v_cvt_scalef32_pk_f32_fp4 v[220:221], v184, 1.0
	v_pk_fma_f32 v[66:67], v[220:221], v[216:217], v[66:67] op_sel_hi:[1,0,1]
	v_cvt_scalef32_pk_f32_fp4 v[222:223], v184, 1.0 op_sel:[1,0,0]
	v_pk_fma_f32 v[64:65], v[222:223], v[216:217], v[64:65] op_sel_hi:[1,0,1]
	v_cvt_scalef32_pk_f32_fp4 v[224:225], v184, 1.0 op_sel:[0,1,0]
	v_pk_fma_f32 v[62:63], v[224:225], v[216:217], v[62:63] op_sel_hi:[1,0,1]
	v_cvt_scalef32_pk_f32_fp4 v[226:227], v184, 1.0 op_sel:[1,1,0]
	v_pk_fma_f32 v[60:61], v[226:227], v[216:217], v[60:61] op_sel_hi:[1,0,1]
	v_cvt_scalef32_pk_f32_fp4 v[220:221], v185, 1.0
	v_pk_fma_f32 v[58:59], v[220:221], v[216:217], v[58:59] op_sel_hi:[1,0,1]
	v_cvt_scalef32_pk_f32_fp4 v[222:223], v185, 1.0 op_sel:[1,0,0]
	v_pk_fma_f32 v[56:57], v[222:223], v[216:217], v[56:57] op_sel_hi:[1,0,1]
	v_cvt_scalef32_pk_f32_fp4 v[224:225], v185, 1.0 op_sel:[0,1,0]
	v_pk_fma_f32 v[54:55], v[224:225], v[216:217], v[54:55] op_sel_hi:[1,0,1]
	v_cvt_scalef32_pk_f32_fp4 v[226:227], v185, 1.0 op_sel:[1,1,0]
	v_pk_fma_f32 v[52:53], v[226:227], v[216:217], v[52:53] op_sel_hi:[1,0,1]
	v_cvt_scalef32_pk_f32_fp4 v[220:221], v186, 1.0
	v_pk_fma_f32 v[50:51], v[220:221], v[216:217], v[50:51] op_sel_hi:[1,0,1]
	v_cvt_scalef32_pk_f32_fp4 v[222:223], v186, 1.0 op_sel:[1,0,0]
	v_pk_fma_f32 v[46:47], v[222:223], v[216:217], v[46:47] op_sel_hi:[1,0,1]
	v_cvt_scalef32_pk_f32_fp4 v[224:225], v186, 1.0 op_sel:[0,1,0]
	v_pk_fma_f32 v[44:45], v[224:225], v[216:217], v[44:45] op_sel_hi:[1,0,1]
	v_cvt_scalef32_pk_f32_fp4 v[226:227], v186, 1.0 op_sel:[1,1,0]
	v_pk_fma_f32 v[42:43], v[226:227], v[216:217], v[42:43] op_sel_hi:[1,0,1]
	v_cvt_scalef32_pk_f32_fp4 v[220:221], v187, 1.0
	v_pk_fma_f32 v[40:41], v[220:221], v[216:217], v[40:41] op_sel_hi:[1,0,1]
	v_cvt_scalef32_pk_f32_fp4 v[222:223], v187, 1.0 op_sel:[1,0,0]
	v_pk_fma_f32 v[38:39], v[222:223], v[216:217], v[38:39] op_sel_hi:[1,0,1]
	v_cvt_scalef32_pk_f32_fp4 v[224:225], v187, 1.0 op_sel:[0,1,0]
	v_pk_fma_f32 v[36:37], v[224:225], v[216:217], v[36:37] op_sel_hi:[1,0,1]
	v_cvt_scalef32_pk_f32_fp4 v[226:227], v187, 1.0 op_sel:[1,1,0]
	v_pk_fma_f32 v[34:35], v[226:227], v[216:217], v[34:35] op_sel_hi:[1,0,1]
	s_waitcnt vmcnt(4)
	v_cvt_scalef32_pk_f32_fp4 v[220:221], v188, 1.0
	v_pk_fma_f32 v[96:97], v[220:221], v[216:217], v[96:97] op_sel:[0,1,0] op_sel_hi:[1,1,1]
	v_cvt_scalef32_pk_f32_fp4 v[222:223], v188, 1.0 op_sel:[1,0,0]
	v_pk_fma_f32 v[98:99], v[222:223], v[216:217], v[98:99] op_sel:[0,1,0] op_sel_hi:[1,1,1]
	v_cvt_scalef32_pk_f32_fp4 v[224:225], v188, 1.0 op_sel:[0,1,0]
	v_pk_fma_f32 v[94:95], v[224:225], v[216:217], v[94:95] op_sel:[0,1,0] op_sel_hi:[1,1,1]
	v_cvt_scalef32_pk_f32_fp4 v[226:227], v188, 1.0 op_sel:[1,1,0]
	v_pk_fma_f32 v[92:93], v[226:227], v[216:217], v[92:93] op_sel:[0,1,0] op_sel_hi:[1,1,1]
	v_cvt_scalef32_pk_f32_fp4 v[220:221], v189, 1.0
	v_pk_fma_f32 v[90:91], v[220:221], v[216:217], v[90:91] op_sel:[0,1,0] op_sel_hi:[1,1,1]
	v_cvt_scalef32_pk_f32_fp4 v[222:223], v189, 1.0 op_sel:[1,0,0]
	v_pk_fma_f32 v[88:89], v[222:223], v[216:217], v[88:89] op_sel:[0,1,0] op_sel_hi:[1,1,1]
	v_cvt_scalef32_pk_f32_fp4 v[224:225], v189, 1.0 op_sel:[0,1,0]
	v_pk_fma_f32 v[86:87], v[224:225], v[216:217], v[86:87] op_sel:[0,1,0] op_sel_hi:[1,1,1]
	v_cvt_scalef32_pk_f32_fp4 v[226:227], v189, 1.0 op_sel:[1,1,0]
	v_pk_fma_f32 v[84:85], v[226:227], v[216:217], v[84:85] op_sel:[0,1,0] op_sel_hi:[1,1,1]
	v_cvt_scalef32_pk_f32_fp4 v[220:221], v190, 1.0
	v_pk_fma_f32 v[82:83], v[220:221], v[216:217], v[82:83] op_sel:[0,1,0] op_sel_hi:[1,1,1]
	v_cvt_scalef32_pk_f32_fp4 v[222:223], v190, 1.0 op_sel:[1,0,0]
	v_pk_fma_f32 v[80:81], v[222:223], v[216:217], v[80:81] op_sel:[0,1,0] op_sel_hi:[1,1,1]
	v_cvt_scalef32_pk_f32_fp4 v[224:225], v190, 1.0 op_sel:[0,1,0]
	v_pk_fma_f32 v[78:79], v[224:225], v[216:217], v[78:79] op_sel:[0,1,0] op_sel_hi:[1,1,1]
	v_cvt_scalef32_pk_f32_fp4 v[226:227], v190, 1.0 op_sel:[1,1,0]
	v_pk_fma_f32 v[76:77], v[226:227], v[216:217], v[76:77] op_sel:[0,1,0] op_sel_hi:[1,1,1]
	v_cvt_scalef32_pk_f32_fp4 v[220:221], v191, 1.0
	v_pk_fma_f32 v[74:75], v[220:221], v[216:217], v[74:75] op_sel:[0,1,0] op_sel_hi:[1,1,1]
	v_cvt_scalef32_pk_f32_fp4 v[222:223], v191, 1.0 op_sel:[1,0,0]
	v_pk_fma_f32 v[72:73], v[222:223], v[216:217], v[72:73] op_sel:[0,1,0] op_sel_hi:[1,1,1]
	v_cvt_scalef32_pk_f32_fp4 v[224:225], v191, 1.0 op_sel:[0,1,0]
	v_pk_fma_f32 v[70:71], v[224:225], v[216:217], v[70:71] op_sel:[0,1,0] op_sel_hi:[1,1,1]
	v_cvt_scalef32_pk_f32_fp4 v[226:227], v191, 1.0 op_sel:[1,1,0]
	v_pk_fma_f32 v[68:69], v[226:227], v[216:217], v[68:69] op_sel:[0,1,0] op_sel_hi:[1,1,1]
	v_cvt_scalef32_pk_f32_fp4 v[220:221], v192, 1.0
	v_pk_fma_f32 v[66:67], v[220:221], v[216:217], v[66:67] op_sel:[0,1,0] op_sel_hi:[1,1,1]
	v_cvt_scalef32_pk_f32_fp4 v[222:223], v192, 1.0 op_sel:[1,0,0]
	v_pk_fma_f32 v[64:65], v[222:223], v[216:217], v[64:65] op_sel:[0,1,0] op_sel_hi:[1,1,1]
	v_cvt_scalef32_pk_f32_fp4 v[224:225], v192, 1.0 op_sel:[0,1,0]
	v_pk_fma_f32 v[62:63], v[224:225], v[216:217], v[62:63] op_sel:[0,1,0] op_sel_hi:[1,1,1]
	v_cvt_scalef32_pk_f32_fp4 v[226:227], v192, 1.0 op_sel:[1,1,0]
	v_pk_fma_f32 v[60:61], v[226:227], v[216:217], v[60:61] op_sel:[0,1,0] op_sel_hi:[1,1,1]
	v_cvt_scalef32_pk_f32_fp4 v[220:221], v193, 1.0
	v_pk_fma_f32 v[58:59], v[220:221], v[216:217], v[58:59] op_sel:[0,1,0] op_sel_hi:[1,1,1]
	v_cvt_scalef32_pk_f32_fp4 v[222:223], v193, 1.0 op_sel:[1,0,0]
	v_pk_fma_f32 v[56:57], v[222:223], v[216:217], v[56:57] op_sel:[0,1,0] op_sel_hi:[1,1,1]
	v_cvt_scalef32_pk_f32_fp4 v[224:225], v193, 1.0 op_sel:[0,1,0]
	v_pk_fma_f32 v[54:55], v[224:225], v[216:217], v[54:55] op_sel:[0,1,0] op_sel_hi:[1,1,1]
	v_cvt_scalef32_pk_f32_fp4 v[226:227], v193, 1.0 op_sel:[1,1,0]
	v_pk_fma_f32 v[52:53], v[226:227], v[216:217], v[52:53] op_sel:[0,1,0] op_sel_hi:[1,1,1]
	v_cvt_scalef32_pk_f32_fp4 v[220:221], v194, 1.0
	v_pk_fma_f32 v[50:51], v[220:221], v[216:217], v[50:51] op_sel:[0,1,0] op_sel_hi:[1,1,1]
	v_cvt_scalef32_pk_f32_fp4 v[222:223], v194, 1.0 op_sel:[1,0,0]
	v_pk_fma_f32 v[46:47], v[222:223], v[216:217], v[46:47] op_sel:[0,1,0] op_sel_hi:[1,1,1]
	v_cvt_scalef32_pk_f32_fp4 v[224:225], v194, 1.0 op_sel:[0,1,0]
	v_pk_fma_f32 v[44:45], v[224:225], v[216:217], v[44:45] op_sel:[0,1,0] op_sel_hi:[1,1,1]
	v_cvt_scalef32_pk_f32_fp4 v[226:227], v194, 1.0 op_sel:[1,1,0]
	v_pk_fma_f32 v[42:43], v[226:227], v[216:217], v[42:43] op_sel:[0,1,0] op_sel_hi:[1,1,1]
	v_cvt_scalef32_pk_f32_fp4 v[220:221], v195, 1.0
	v_pk_fma_f32 v[40:41], v[220:221], v[216:217], v[40:41] op_sel:[0,1,0] op_sel_hi:[1,1,1]
	v_cvt_scalef32_pk_f32_fp4 v[222:223], v195, 1.0 op_sel:[1,0,0]
	v_pk_fma_f32 v[38:39], v[222:223], v[216:217], v[38:39] op_sel:[0,1,0] op_sel_hi:[1,1,1]
	v_cvt_scalef32_pk_f32_fp4 v[224:225], v195, 1.0 op_sel:[0,1,0]
	v_pk_fma_f32 v[36:37], v[224:225], v[216:217], v[36:37] op_sel:[0,1,0] op_sel_hi:[1,1,1]
	v_cvt_scalef32_pk_f32_fp4 v[226:227], v195, 1.0 op_sel:[1,1,0]
	v_pk_fma_f32 v[34:35], v[226:227], v[216:217], v[34:35] op_sel:[0,1,0] op_sel_hi:[1,1,1]
	s_waitcnt vmcnt(2)
	v_cvt_scalef32_pk_f32_fp4 v[220:221], v196, 1.0
	v_pk_fma_f32 v[96:97], v[220:221], v[218:219], v[96:97] op_sel_hi:[1,0,1]
	v_cvt_scalef32_pk_f32_fp4 v[222:223], v196, 1.0 op_sel:[1,0,0]
	v_pk_fma_f32 v[98:99], v[222:223], v[218:219], v[98:99] op_sel_hi:[1,0,1]
	v_cvt_scalef32_pk_f32_fp4 v[224:225], v196, 1.0 op_sel:[0,1,0]
	v_pk_fma_f32 v[94:95], v[224:225], v[218:219], v[94:95] op_sel_hi:[1,0,1]
	v_cvt_scalef32_pk_f32_fp4 v[226:227], v196, 1.0 op_sel:[1,1,0]
	v_pk_fma_f32 v[92:93], v[226:227], v[218:219], v[92:93] op_sel_hi:[1,0,1]
	v_cvt_scalef32_pk_f32_fp4 v[220:221], v197, 1.0
	v_pk_fma_f32 v[90:91], v[220:221], v[218:219], v[90:91] op_sel_hi:[1,0,1]
	v_cvt_scalef32_pk_f32_fp4 v[222:223], v197, 1.0 op_sel:[1,0,0]
	v_pk_fma_f32 v[88:89], v[222:223], v[218:219], v[88:89] op_sel_hi:[1,0,1]
	v_cvt_scalef32_pk_f32_fp4 v[224:225], v197, 1.0 op_sel:[0,1,0]
	v_pk_fma_f32 v[86:87], v[224:225], v[218:219], v[86:87] op_sel_hi:[1,0,1]
	v_cvt_scalef32_pk_f32_fp4 v[226:227], v197, 1.0 op_sel:[1,1,0]
	v_pk_fma_f32 v[84:85], v[226:227], v[218:219], v[84:85] op_sel_hi:[1,0,1]
	v_cvt_scalef32_pk_f32_fp4 v[220:221], v198, 1.0
	v_pk_fma_f32 v[82:83], v[220:221], v[218:219], v[82:83] op_sel_hi:[1,0,1]
	v_cvt_scalef32_pk_f32_fp4 v[222:223], v198, 1.0 op_sel:[1,0,0]
	v_pk_fma_f32 v[80:81], v[222:223], v[218:219], v[80:81] op_sel_hi:[1,0,1]
	v_cvt_scalef32_pk_f32_fp4 v[224:225], v198, 1.0 op_sel:[0,1,0]
	v_pk_fma_f32 v[78:79], v[224:225], v[218:219], v[78:79] op_sel_hi:[1,0,1]
	v_cvt_scalef32_pk_f32_fp4 v[226:227], v198, 1.0 op_sel:[1,1,0]
	v_pk_fma_f32 v[76:77], v[226:227], v[218:219], v[76:77] op_sel_hi:[1,0,1]
	v_cvt_scalef32_pk_f32_fp4 v[220:221], v199, 1.0
	v_pk_fma_f32 v[74:75], v[220:221], v[218:219], v[74:75] op_sel_hi:[1,0,1]
	v_cvt_scalef32_pk_f32_fp4 v[222:223], v199, 1.0 op_sel:[1,0,0]
	v_pk_fma_f32 v[72:73], v[222:223], v[218:219], v[72:73] op_sel_hi:[1,0,1]
	v_cvt_scalef32_pk_f32_fp4 v[224:225], v199, 1.0 op_sel:[0,1,0]
	v_pk_fma_f32 v[70:71], v[224:225], v[218:219], v[70:71] op_sel_hi:[1,0,1]
	v_cvt_scalef32_pk_f32_fp4 v[226:227], v199, 1.0 op_sel:[1,1,0]
	v_pk_fma_f32 v[68:69], v[226:227], v[218:219], v[68:69] op_sel_hi:[1,0,1]
	v_cvt_scalef32_pk_f32_fp4 v[220:221], v200, 1.0
	v_pk_fma_f32 v[66:67], v[220:221], v[218:219], v[66:67] op_sel_hi:[1,0,1]
	v_cvt_scalef32_pk_f32_fp4 v[222:223], v200, 1.0 op_sel:[1,0,0]
	v_pk_fma_f32 v[64:65], v[222:223], v[218:219], v[64:65] op_sel_hi:[1,0,1]
	v_cvt_scalef32_pk_f32_fp4 v[224:225], v200, 1.0 op_sel:[0,1,0]
	v_pk_fma_f32 v[62:63], v[224:225], v[218:219], v[62:63] op_sel_hi:[1,0,1]
	v_cvt_scalef32_pk_f32_fp4 v[226:227], v200, 1.0 op_sel:[1,1,0]
	v_pk_fma_f32 v[60:61], v[226:227], v[218:219], v[60:61] op_sel_hi:[1,0,1]
	v_cvt_scalef32_pk_f32_fp4 v[220:221], v201, 1.0
	v_pk_fma_f32 v[58:59], v[220:221], v[218:219], v[58:59] op_sel_hi:[1,0,1]
	v_cvt_scalef32_pk_f32_fp4 v[222:223], v201, 1.0 op_sel:[1,0,0]
	v_pk_fma_f32 v[56:57], v[222:223], v[218:219], v[56:57] op_sel_hi:[1,0,1]
	v_cvt_scalef32_pk_f32_fp4 v[224:225], v201, 1.0 op_sel:[0,1,0]
	v_pk_fma_f32 v[54:55], v[224:225], v[218:219], v[54:55] op_sel_hi:[1,0,1]
	v_cvt_scalef32_pk_f32_fp4 v[226:227], v201, 1.0 op_sel:[1,1,0]
	v_pk_fma_f32 v[52:53], v[226:227], v[218:219], v[52:53] op_sel_hi:[1,0,1]
	v_cvt_scalef32_pk_f32_fp4 v[220:221], v202, 1.0
	v_pk_fma_f32 v[50:51], v[220:221], v[218:219], v[50:51] op_sel_hi:[1,0,1]
	v_cvt_scalef32_pk_f32_fp4 v[222:223], v202, 1.0 op_sel:[1,0,0]
	v_pk_fma_f32 v[46:47], v[222:223], v[218:219], v[46:47] op_sel_hi:[1,0,1]
	v_cvt_scalef32_pk_f32_fp4 v[224:225], v202, 1.0 op_sel:[0,1,0]
	v_pk_fma_f32 v[44:45], v[224:225], v[218:219], v[44:45] op_sel_hi:[1,0,1]
	v_cvt_scalef32_pk_f32_fp4 v[226:227], v202, 1.0 op_sel:[1,1,0]
	v_pk_fma_f32 v[42:43], v[226:227], v[218:219], v[42:43] op_sel_hi:[1,0,1]
	v_cvt_scalef32_pk_f32_fp4 v[220:221], v203, 1.0
	v_pk_fma_f32 v[40:41], v[220:221], v[218:219], v[40:41] op_sel_hi:[1,0,1]
	v_cvt_scalef32_pk_f32_fp4 v[222:223], v203, 1.0 op_sel:[1,0,0]
	v_pk_fma_f32 v[38:39], v[222:223], v[218:219], v[38:39] op_sel_hi:[1,0,1]
	v_cvt_scalef32_pk_f32_fp4 v[224:225], v203, 1.0 op_sel:[0,1,0]
	v_pk_fma_f32 v[36:37], v[224:225], v[218:219], v[36:37] op_sel_hi:[1,0,1]
	v_cvt_scalef32_pk_f32_fp4 v[226:227], v203, 1.0 op_sel:[1,1,0]
	v_pk_fma_f32 v[34:35], v[226:227], v[218:219], v[34:35] op_sel_hi:[1,0,1]
	s_waitcnt vmcnt(0)
	v_cvt_scalef32_pk_f32_fp4 v[220:221], v204, 1.0
	v_pk_fma_f32 v[96:97], v[220:221], v[218:219], v[96:97] op_sel:[0,1,0] op_sel_hi:[1,1,1]
	v_cvt_scalef32_pk_f32_fp4 v[222:223], v204, 1.0 op_sel:[1,0,0]
	v_pk_fma_f32 v[98:99], v[222:223], v[218:219], v[98:99] op_sel:[0,1,0] op_sel_hi:[1,1,1]
	v_cvt_scalef32_pk_f32_fp4 v[224:225], v204, 1.0 op_sel:[0,1,0]
	v_pk_fma_f32 v[94:95], v[224:225], v[218:219], v[94:95] op_sel:[0,1,0] op_sel_hi:[1,1,1]
	v_cvt_scalef32_pk_f32_fp4 v[226:227], v204, 1.0 op_sel:[1,1,0]
	v_pk_fma_f32 v[92:93], v[226:227], v[218:219], v[92:93] op_sel:[0,1,0] op_sel_hi:[1,1,1]
	v_cvt_scalef32_pk_f32_fp4 v[220:221], v205, 1.0
	v_pk_fma_f32 v[90:91], v[220:221], v[218:219], v[90:91] op_sel:[0,1,0] op_sel_hi:[1,1,1]
	v_cvt_scalef32_pk_f32_fp4 v[222:223], v205, 1.0 op_sel:[1,0,0]
	v_pk_fma_f32 v[88:89], v[222:223], v[218:219], v[88:89] op_sel:[0,1,0] op_sel_hi:[1,1,1]
	v_cvt_scalef32_pk_f32_fp4 v[224:225], v205, 1.0 op_sel:[0,1,0]
	v_pk_fma_f32 v[86:87], v[224:225], v[218:219], v[86:87] op_sel:[0,1,0] op_sel_hi:[1,1,1]
	v_cvt_scalef32_pk_f32_fp4 v[226:227], v205, 1.0 op_sel:[1,1,0]
	v_pk_fma_f32 v[84:85], v[226:227], v[218:219], v[84:85] op_sel:[0,1,0] op_sel_hi:[1,1,1]
	v_cvt_scalef32_pk_f32_fp4 v[220:221], v206, 1.0
	v_pk_fma_f32 v[82:83], v[220:221], v[218:219], v[82:83] op_sel:[0,1,0] op_sel_hi:[1,1,1]
	v_cvt_scalef32_pk_f32_fp4 v[222:223], v206, 1.0 op_sel:[1,0,0]
	v_pk_fma_f32 v[80:81], v[222:223], v[218:219], v[80:81] op_sel:[0,1,0] op_sel_hi:[1,1,1]
	v_cvt_scalef32_pk_f32_fp4 v[224:225], v206, 1.0 op_sel:[0,1,0]
	v_pk_fma_f32 v[78:79], v[224:225], v[218:219], v[78:79] op_sel:[0,1,0] op_sel_hi:[1,1,1]
	v_cvt_scalef32_pk_f32_fp4 v[226:227], v206, 1.0 op_sel:[1,1,0]
	v_pk_fma_f32 v[76:77], v[226:227], v[218:219], v[76:77] op_sel:[0,1,0] op_sel_hi:[1,1,1]
	v_cvt_scalef32_pk_f32_fp4 v[220:221], v207, 1.0
	v_pk_fma_f32 v[74:75], v[220:221], v[218:219], v[74:75] op_sel:[0,1,0] op_sel_hi:[1,1,1]
	v_cvt_scalef32_pk_f32_fp4 v[222:223], v207, 1.0 op_sel:[1,0,0]
	v_pk_fma_f32 v[72:73], v[222:223], v[218:219], v[72:73] op_sel:[0,1,0] op_sel_hi:[1,1,1]
	v_cvt_scalef32_pk_f32_fp4 v[224:225], v207, 1.0 op_sel:[0,1,0]
	v_pk_fma_f32 v[70:71], v[224:225], v[218:219], v[70:71] op_sel:[0,1,0] op_sel_hi:[1,1,1]
	v_cvt_scalef32_pk_f32_fp4 v[226:227], v207, 1.0 op_sel:[1,1,0]
	v_pk_fma_f32 v[68:69], v[226:227], v[218:219], v[68:69] op_sel:[0,1,0] op_sel_hi:[1,1,1]
	v_cvt_scalef32_pk_f32_fp4 v[220:221], v208, 1.0
	v_pk_fma_f32 v[66:67], v[220:221], v[218:219], v[66:67] op_sel:[0,1,0] op_sel_hi:[1,1,1]
	v_cvt_scalef32_pk_f32_fp4 v[222:223], v208, 1.0 op_sel:[1,0,0]
	v_pk_fma_f32 v[64:65], v[222:223], v[218:219], v[64:65] op_sel:[0,1,0] op_sel_hi:[1,1,1]
	v_cvt_scalef32_pk_f32_fp4 v[224:225], v208, 1.0 op_sel:[0,1,0]
	v_pk_fma_f32 v[62:63], v[224:225], v[218:219], v[62:63] op_sel:[0,1,0] op_sel_hi:[1,1,1]
	v_cvt_scalef32_pk_f32_fp4 v[226:227], v208, 1.0 op_sel:[1,1,0]
	v_pk_fma_f32 v[60:61], v[226:227], v[218:219], v[60:61] op_sel:[0,1,0] op_sel_hi:[1,1,1]
	v_cvt_scalef32_pk_f32_fp4 v[220:221], v209, 1.0
	v_pk_fma_f32 v[58:59], v[220:221], v[218:219], v[58:59] op_sel:[0,1,0] op_sel_hi:[1,1,1]
	v_cvt_scalef32_pk_f32_fp4 v[222:223], v209, 1.0 op_sel:[1,0,0]
	v_pk_fma_f32 v[56:57], v[222:223], v[218:219], v[56:57] op_sel:[0,1,0] op_sel_hi:[1,1,1]
	v_cvt_scalef32_pk_f32_fp4 v[224:225], v209, 1.0 op_sel:[0,1,0]
	v_pk_fma_f32 v[54:55], v[224:225], v[218:219], v[54:55] op_sel:[0,1,0] op_sel_hi:[1,1,1]
	v_cvt_scalef32_pk_f32_fp4 v[226:227], v209, 1.0 op_sel:[1,1,0]
	v_pk_fma_f32 v[52:53], v[226:227], v[218:219], v[52:53] op_sel:[0,1,0] op_sel_hi:[1,1,1]
	v_cvt_scalef32_pk_f32_fp4 v[220:221], v210, 1.0
	v_pk_fma_f32 v[50:51], v[220:221], v[218:219], v[50:51] op_sel:[0,1,0] op_sel_hi:[1,1,1]
	v_cvt_scalef32_pk_f32_fp4 v[222:223], v210, 1.0 op_sel:[1,0,0]
	v_pk_fma_f32 v[46:47], v[222:223], v[218:219], v[46:47] op_sel:[0,1,0] op_sel_hi:[1,1,1]
	v_cvt_scalef32_pk_f32_fp4 v[224:225], v210, 1.0 op_sel:[0,1,0]
	v_pk_fma_f32 v[44:45], v[224:225], v[218:219], v[44:45] op_sel:[0,1,0] op_sel_hi:[1,1,1]
	v_cvt_scalef32_pk_f32_fp4 v[226:227], v210, 1.0 op_sel:[1,1,0]
	v_pk_fma_f32 v[42:43], v[226:227], v[218:219], v[42:43] op_sel:[0,1,0] op_sel_hi:[1,1,1]
	v_cvt_scalef32_pk_f32_fp4 v[220:221], v211, 1.0
	v_pk_fma_f32 v[40:41], v[220:221], v[218:219], v[40:41] op_sel:[0,1,0] op_sel_hi:[1,1,1]
	v_cvt_scalef32_pk_f32_fp4 v[222:223], v211, 1.0 op_sel:[1,0,0]
	v_pk_fma_f32 v[38:39], v[222:223], v[218:219], v[38:39] op_sel:[0,1,0] op_sel_hi:[1,1,1]
	v_cvt_scalef32_pk_f32_fp4 v[224:225], v211, 1.0 op_sel:[0,1,0]
	v_pk_fma_f32 v[36:37], v[224:225], v[218:219], v[36:37] op_sel:[0,1,0] op_sel_hi:[1,1,1]
	v_cvt_scalef32_pk_f32_fp4 v[226:227], v211, 1.0 op_sel:[1,1,0]
	v_pk_fma_f32 v[34:35], v[226:227], v[218:219], v[34:35] op_sel:[0,1,0] op_sel_hi:[1,1,1]
	s_add_i32 s0, s9, s8
	v_mov_b32_e32 v48, v145
	s_ashr_i32 s1, s0, 31
	s_lshl_b64 s[10:11], s[0:1], 13
	s_waitcnt vmcnt(1)
	v_lshlrev_b32_e32 v22, 2, v48
	s_add_u32 s10, s28, s10
	v_add_u32_e32 v24, 0x800, v22
	v_add_u32_e32 v26, 0x900, v22
	s_addc_u32 s11, s29, s11
	v_ashrrev_i32_e32 v23, 31, v22
	v_ashrrev_i32_e32 v25, 31, v24
	v_ashrrev_i32_e32 v27, 31, v26
	v_lshl_add_u64 v[0:1], v[22:23], 1, s[10:11]
	v_lshl_add_u64 v[16:17], v[24:25], 1, s[10:11]
	v_lshl_add_u64 v[18:19], v[26:27], 1, s[10:11]
	global_load_dwordx2 v[2:3], v[0:1], off nt
	global_load_dwordx2 v[4:5], v[0:1], off offset:512 nt
	global_load_dwordx2 v[6:7], v[0:1], off offset:1024 nt
	global_load_dwordx2 v[8:9], v[0:1], off offset:1536 nt
	global_load_dwordx2 v[10:11], v[0:1], off offset:2048 nt
	global_load_dwordx2 v[12:13], v[0:1], off offset:2560 nt
	global_load_dwordx2 v[14:15], v[0:1], off offset:3072 nt
	s_nop 0
	global_load_dwordx2 v[0:1], v[0:1], off offset:3584 nt
	v_add_u32_e32 v28, 0xa00, v22
	global_load_dwordx2 v[16:17], v[16:17], off
	v_ashrrev_i32_e32 v29, 31, v28
	global_load_dwordx2 v[18:19], v[18:19], off
	v_add_u32_e32 v30, 0xb00, v22
	v_lshl_add_u64 v[20:21], v[28:29], 1, s[10:11]
	v_ashrrev_i32_e32 v31, 31, v30
	v_add_u32_e32 v102, 0xc00, v22
	global_load_dwordx2 v[112:113], v[20:21], off
	v_lshl_add_u64 v[20:21], v[30:31], 1, s[10:11]
	v_ashrrev_i32_e32 v103, 31, v102
	v_add_u32_e32 v100, 0xd00, v22
	global_load_dwordx2 v[114:115], v[20:21], off
	v_lshl_add_u64 v[20:21], v[102:103], 1, s[10:11]
	v_ashrrev_i32_e32 v101, 31, v100
	v_add_u32_e32 v104, 0xe00, v22
	global_load_dwordx2 v[116:117], v[20:21], off
	v_lshl_add_u64 v[20:21], v[100:101], 1, s[10:11]
	v_ashrrev_i32_e32 v105, 31, v104
	global_load_dwordx2 v[118:119], v[20:21], off
	v_lshl_add_u64 v[20:21], v[104:105], 1, s[10:11]
	global_load_dwordx2 v[192:193], v[20:21], off
	v_add_u32_e32 v20, 0xf00, v22
	v_ashrrev_i32_e32 v21, 31, v20
	v_lshl_add_u64 v[110:111], v[20:21], 1, s[10:11]
	global_load_dwordx2 v[194:195], v[110:111], off
	v_lshl_add_u32 v48, v48, 4, 0
	v_add_u32_e32 v147, 0x10100, v48
	ds_read_b128 v[148:151], v147
	ds_read_b128 v[152:155], v147 offset:1024
	ds_read_b128 v[156:159], v147 offset:2048
	ds_read_b128 v[160:163], v147 offset:3072
	ds_read_b128 v[164:167], v147 offset:4096
	ds_read_b128 v[168:171], v147 offset:5120
	ds_read_b128 v[172:175], v147 offset:6144
	ds_read_b128 v[176:179], v147 offset:7168
	ds_read_b128 v[180:183], v147 offset:8192
	ds_read_b128 v[184:187], v147 offset:9216
	s_lshl_b64 s[0:1], s[0:1], 14
	s_add_u32 s10, s52, s0
	s_addc_u32 s11, s53, s1
	v_add_u32_e32 v108, 0x400, v22
	v_add_u32_e32 v106, 0x500, v22
	v_add_u32_e32 v110, 0x600, v22
	v_ashrrev_i32_e32 v109, 31, v108
	v_ashrrev_i32_e32 v107, 31, v106
	v_lshl_add_u64 v[30:31], v[30:31], 2, s[10:11]
	v_lshl_add_u64 v[100:101], v[100:101], 2, s[10:11]
	s_mov_b32 s9, 1
	v_lshl_add_u64 v[102:103], v[102:103], 2, s[10:11]
	v_lshl_add_u64 v[104:105], v[104:105], 2, s[10:11]
	s_waitcnt vmcnt(15)
	v_lshlrev_b32_e32 v196, 16, v2
	v_and_b32_e32 v197, 0xffff0000, v2
	s_waitcnt vmcnt(14)
	v_lshlrev_b32_e32 v200, 16, v4
	v_and_b32_e32 v201, 0xffff0000, v4
	v_lshlrev_b32_e32 v198, 16, v3
	v_and_b32_e32 v199, 0xffff0000, v3
	v_lshlrev_b32_e32 v202, 16, v5
	v_and_b32_e32 v203, 0xffff0000, v5
	s_waitcnt vmcnt(13)
	v_lshlrev_b32_e32 v204, 16, v6
	v_and_b32_e32 v205, 0xffff0000, v6
	v_lshlrev_b32_e32 v206, 16, v7
	v_and_b32_e32 v207, 0xffff0000, v7
	s_waitcnt vmcnt(12)
	v_lshlrev_b32_e32 v208, 16, v8
	v_and_b32_e32 v209, 0xffff0000, v8
	v_lshlrev_b32_e32 v210, 16, v9
	v_and_b32_e32 v211, 0xffff0000, v9
	s_waitcnt vmcnt(11)
	v_lshlrev_b32_e32 v212, 16, v10
	v_and_b32_e32 v213, 0xffff0000, v10
	v_lshlrev_b32_e32 v214, 16, v11
	v_and_b32_e32 v215, 0xffff0000, v11
	s_waitcnt vmcnt(10)
	v_lshlrev_b32_e32 v216, 16, v12
	v_and_b32_e32 v217, 0xffff0000, v12
	v_lshlrev_b32_e32 v218, 16, v13
	v_and_b32_e32 v219, 0xffff0000, v13
	s_waitcnt vmcnt(9)
	v_lshlrev_b32_e32 v220, 16, v14
	v_and_b32_e32 v221, 0xffff0000, v14
	v_lshlrev_b32_e32 v222, 16, v15
	v_and_b32_e32 v223, 0xffff0000, v15
	s_waitcnt vmcnt(8)
	v_lshlrev_b32_e32 v224, 16, v0
	v_and_b32_e32 v225, 0xffff0000, v0
	v_lshlrev_b32_e32 v226, 16, v1
	v_and_b32_e32 v227, 0xffff0000, v1
	s_waitcnt vmcnt(7)
	v_lshlrev_b32_e32 v228, 16, v16
	v_and_b32_e32 v229, 0xffff0000, v16
	v_lshlrev_b32_e32 v230, 16, v17
	v_and_b32_e32 v231, 0xffff0000, v17
	s_waitcnt vmcnt(6)
	v_lshlrev_b32_e32 v232, 16, v18
	v_and_b32_e32 v233, 0xffff0000, v18
	v_lshlrev_b32_e32 v234, 16, v19
	v_and_b32_e32 v235, 0xffff0000, v19
	ds_read_b128 v[188:191], v147 offset:10240
	ds_read_b128 v[16:19], v147 offset:11264
	ds_read_b128 v[12:15], v147 offset:12288
	ds_read_b128 v[8:11], v147 offset:13312
	ds_read_b128 v[4:7], v147 offset:14336
	ds_read_b128 v[0:3], v147 offset:15360
	s_waitcnt lgkmcnt(14)
	v_pk_fma_f32 v[96:97], v[96:97], v[148:149], v[196:197]
	v_pk_fma_f32 v[94:95], v[94:95], v[152:153], v[200:201]
	v_pk_fma_f32 v[98:99], v[98:99], v[150:151], v[198:199]
	v_pk_fma_f32 v[92:93], v[92:93], v[154:155], v[202:203]
	v_mov_b32_e32 v150, v97
	v_mov_b32_e32 v151, v95
	v_mov_b32_e32 v148, v96
	v_mov_b32_e32 v149, v94
	v_pk_mul_f32 v[150:151], v[150:151], v[150:151]
	v_mov_b32_e32 v152, v99
	v_mov_b32_e32 v153, v93
	v_pk_fma_f32 v[148:149], v[148:149], v[148:149], v[150:151]
	v_mov_b32_e32 v150, v98
	v_mov_b32_e32 v151, v92
	v_pk_mul_f32 v[152:153], v[152:153], v[152:153]
	s_waitcnt lgkmcnt(13)
	v_pk_fma_f32 v[90:91], v[90:91], v[156:157], v[204:205]
	v_pk_fma_f32 v[88:89], v[88:89], v[158:159], v[206:207]
	v_pk_fma_f32 v[150:151], v[150:151], v[150:151], v[152:153]
	v_mov_b32_e32 v152, v91
	v_mov_b32_e32 v153, v89
	s_waitcnt lgkmcnt(12)
	v_pk_fma_f32 v[86:87], v[86:87], v[160:161], v[208:209]
	s_waitcnt lgkmcnt(0)
	v_mul_f32_e32 v36, v36, v0
	v_pk_add_f32 v[148:149], v[148:149], v[150:151]
	v_mov_b32_e32 v150, v90
	v_mov_b32_e32 v151, v88
	v_pk_mul_f32 v[152:153], v[152:153], v[152:153]
	v_mul_f32_e32 v0, v87, v87
	v_pk_fma_f32 v[84:85], v[84:85], v[162:163], v[210:211]
	v_pk_fma_f32 v[150:151], v[150:151], v[150:151], v[152:153]
	v_pk_fma_f32 v[152:153], v[86:87], v[86:87], v[0:1] op_sel_hi:[1,1,0]
	v_mul_f32_e32 v0, v85, v85
	v_pk_fma_f32 v[82:83], v[82:83], v[164:165], v[212:213]
	v_pk_fma_f32 v[80:81], v[80:81], v[166:167], v[214:215]
	v_pk_add_f32 v[148:149], v[148:149], v[148:149] op_sel:[0,1] op_sel_hi:[1,0]
	v_pk_add_f32 v[150:151], v[150:151], v[150:151] op_sel:[0,1] op_sel_hi:[1,0]
	v_pk_fma_f32 v[154:155], v[84:85], v[84:85], v[0:1] op_sel_hi:[1,1,0]
	v_pk_mul_f32 v[156:157], v[82:83], v[82:83]
	v_pk_mul_f32 v[158:159], v[80:81], v[80:81]
	v_mov_b32_e32 v149, v156
	v_mov_b32_e32 v151, v157
	v_mov_b32_e32 v153, v158
	v_mov_b32_e32 v155, v159
	v_pk_fma_f32 v[78:79], v[78:79], v[168:169], v[216:217]
	v_pk_fma_f32 v[76:77], v[76:77], v[170:171], v[218:219]
	v_pk_add_f32 v[148:149], v[148:149], v[150:151]
	v_pk_add_f32 v[150:151], v[152:153], v[154:155]
	v_mov_b32_e32 v152, v79
	v_mov_b32_e32 v153, v77
	v_pk_fma_f32 v[74:75], v[74:75], v[172:173], v[220:221]
	v_pk_add_f32 v[148:149], v[148:149], v[150:151]
	v_mov_b32_e32 v150, v78
	v_mov_b32_e32 v151, v76
	v_pk_mul_f32 v[152:153], v[152:153], v[152:153]
	v_mul_f32_e32 v0, v75, v75
	v_pk_fma_f32 v[72:73], v[72:73], v[174:175], v[222:223]
	v_pk_fma_f32 v[150:151], v[150:151], v[150:151], v[152:153]
	v_pk_fma_f32 v[152:153], v[74:75], v[74:75], v[0:1] op_sel_hi:[1,1,0]
	v_mul_f32_e32 v0, v73, v73
	v_pk_fma_f32 v[70:71], v[70:71], v[176:177], v[224:225]
	v_pk_fma_f32 v[68:69], v[68:69], v[178:179], v[226:227]
	v_pk_add_f32 v[148:149], v[148:149], v[148:149] op_sel:[0,1] op_sel_hi:[1,0]
	v_pk_add_f32 v[150:151], v[150:151], v[150:151] op_sel:[0,1] op_sel_hi:[1,0]
	v_pk_fma_f32 v[154:155], v[72:73], v[72:73], v[0:1] op_sel_hi:[1,1,0]
	v_pk_mul_f32 v[156:157], v[70:71], v[70:71]
	v_pk_mul_f32 v[158:159], v[68:69], v[68:69]
	v_mov_b32_e32 v149, v156
	v_mov_b32_e32 v151, v157
	v_mov_b32_e32 v153, v158
	v_mov_b32_e32 v155, v159
	v_pk_fma_f32 v[66:67], v[66:67], v[180:181], v[228:229]
	v_pk_fma_f32 v[64:65], v[64:65], v[182:183], v[230:231]
	v_pk_add_f32 v[148:149], v[148:149], v[150:151]
	v_pk_add_f32 v[150:151], v[152:153], v[154:155]
	v_mov_b32_e32 v152, v67
	v_mov_b32_e32 v153, v65
	v_pk_fma_f32 v[62:63], v[62:63], v[184:185], v[232:233]
	s_waitcnt vmcnt(5)
	v_lshlrev_b32_e32 v236, 16, v112
	v_and_b32_e32 v237, 0xffff0000, v112
	v_lshlrev_b32_e32 v238, 16, v113
	v_and_b32_e32 v239, 0xffff0000, v113
	v_pk_add_f32 v[148:149], v[148:149], v[150:151]
	v_mov_b32_e32 v150, v66
	v_mov_b32_e32 v151, v64
	v_pk_mul_f32 v[152:153], v[152:153], v[152:153]
	v_mul_f32_e32 v0, v63, v63
	v_pk_fma_f32 v[60:61], v[60:61], v[186:187], v[234:235]
	s_waitcnt vmcnt(4)
	v_lshlrev_b32_e32 v130, 16, v114
	v_and_b32_e32 v131, 0xffff0000, v114
	v_lshlrev_b32_e32 v128, 16, v115
	v_and_b32_e32 v129, 0xffff0000, v115
	v_pk_fma_f32 v[150:151], v[150:151], v[150:151], v[152:153]
	v_pk_fma_f32 v[152:153], v[62:63], v[62:63], v[0:1] op_sel_hi:[1,1,0]
	v_mul_f32_e32 v0, v61, v61
	v_pk_fma_f32 v[58:59], v[58:59], v[188:189], v[236:237]
	v_pk_fma_f32 v[56:57], v[56:57], v[190:191], v[238:239]
	s_waitcnt vmcnt(3)
	v_lshlrev_b32_e32 v126, 16, v116
	v_and_b32_e32 v127, 0xffff0000, v116
	v_pk_add_f32 v[148:149], v[148:149], v[148:149] op_sel:[0,1] op_sel_hi:[1,0]
	v_pk_add_f32 v[150:151], v[150:151], v[150:151] op_sel:[0,1] op_sel_hi:[1,0]
	v_pk_fma_f32 v[154:155], v[60:61], v[60:61], v[0:1] op_sel_hi:[1,1,0]
	v_pk_mul_f32 v[156:157], v[58:59], v[58:59]
	v_pk_mul_f32 v[158:159], v[56:57], v[56:57]
	v_pk_fma_f32 v[16:17], v[54:55], v[16:17], v[130:131]
	v_pk_fma_f32 v[18:19], v[52:53], v[18:19], v[128:129]
	v_lshlrev_b32_e32 v124, 16, v117
	v_and_b32_e32 v125, 0xffff0000, v117
	v_mov_b32_e32 v149, v156
	v_mov_b32_e32 v151, v157
	v_mov_b32_e32 v153, v158
	v_mov_b32_e32 v155, v159
	v_mov_b32_e32 v54, v17
	v_mov_b32_e32 v55, v19
	v_pk_fma_f32 v[12:13], v[50:51], v[12:13], v[126:127]
	v_pk_add_f32 v[148:149], v[148:149], v[150:151]
	v_pk_add_f32 v[150:151], v[152:153], v[154:155]
	v_mov_b32_e32 v52, v16
	v_mov_b32_e32 v53, v18
	v_pk_mul_f32 v[54:55], v[54:55], v[54:55]
	v_mul_f32_e32 v0, v13, v13
	v_pk_fma_f32 v[14:15], v[46:47], v[14:15], v[124:125]
	s_waitcnt vmcnt(2)
	v_lshlrev_b32_e32 v122, 16, v118
	v_and_b32_e32 v123, 0xffff0000, v118
	v_lshlrev_b32_e32 v120, 16, v119
	v_and_b32_e32 v121, 0xffff0000, v119
	s_waitcnt vmcnt(1)
	v_lshlrev_b32_e32 v118, 16, v192
	v_and_b32_e32 v119, 0xffff0000, v192
	v_pk_add_f32 v[148:149], v[148:149], v[150:151]
	v_pk_fma_f32 v[52:53], v[52:53], v[52:53], v[54:55]
	v_pk_fma_f32 v[50:51], v[12:13], v[12:13], v[0:1] op_sel_hi:[1,1,0]
	v_mul_f32_e32 v0, v15, v15
	v_lshlrev_b32_e32 v116, 16, v193
	v_and_b32_e32 v117, 0xffff0000, v193
	s_waitcnt vmcnt(0)
	v_lshlrev_b32_e32 v111, 16, v194
	v_pk_fma_f32 v[46:47], v[14:15], v[14:15], v[0:1] op_sel_hi:[1,1,0]
	v_pk_fma_f32 v[8:9], v[44:45], v[8:9], v[122:123]
	v_pk_fma_f32 v[4:5], v[40:41], v[4:5], v[118:119]
	v_pk_add_f32 v[44:45], v[148:149], v[148:149] op_sel:[0,1] op_sel_hi:[1,0]
	v_pk_add_f32 v[52:53], v[52:53], v[52:53] op_sel:[0,1] op_sel_hi:[1,0]
	v_mul_f32_e32 v0, v5, v5
	v_pk_fma_f32 v[6:7], v[38:39], v[6:7], v[116:117]
	v_mov_b32_e32 v45, v36
	v_mov_b32_e32 v53, v111
	v_mov_b32_e32 v51, v36
	v_mov_b32_e32 v47, v111
	v_pk_fma_f32 v[10:11], v[42:43], v[10:11], v[120:121]
	v_pk_fma_f32 v[40:41], v[4:5], v[4:5], v[0:1] op_sel_hi:[1,1,0]
	v_mul_f32_e32 v0, v7, v7
	v_pk_add_f32 v[54:55], v[44:45], v[52:53]
	v_pk_add_f32 v[44:45], v[50:51], v[46:47]
	v_and_b32_e32 v115, 0xffff0000, v194
	v_pk_mul_f32 v[42:43], v[10:11], v[10:11]
	v_pk_fma_f32 v[38:39], v[6:7], v[6:7], v[0:1] op_sel_hi:[1,1,0]
	v_pk_add_f32 v[46:47], v[54:55], v[44:45]
	v_pk_mul_f32 v[44:45], v[54:55], v[44:45]
	v_mov_b32_e32 v36, v8
	v_mov_b32_e32 v0, v8
	v_mul_f32_e32 v114, v9, v9
	v_lshlrev_b32_e32 v112, 16, v195
	v_and_b32_e32 v113, 0xffff0000, v195
	v_mov_b32_e32 v47, v45
	v_mov_b32_e32 v44, v10
	v_mov_b32_e32 v45, v37
	v_mov_b32_e32 v50, v10
	v_mov_b32_e32 v51, v1
	v_pk_fma_f32 v[0:1], v[36:37], v[0:1], v[114:115]
	v_mov_b32_e32 v114, v43
	v_pk_fma_f32 v[36:37], v[44:45], v[50:51], v[114:115]
	v_pk_fma_f32 v[2:3], v[34:35], v[2:3], v[112:113]
	v_pk_add_f32 v[42:43], v[0:1], v[36:37]
	v_pk_mul_f32 v[36:37], v[0:1], v[36:37]
	v_pk_mul_f32 v[34:35], v[2:3], v[2:3]
	v_mov_b32_e32 v43, v37
	v_mov_b32_e32 v41, v34
	v_mov_b32_e32 v39, v35
	v_pk_add_f32 v[36:37], v[46:47], v[42:43]
	v_pk_add_f32 v[34:35], v[40:41], v[38:39]
	v_add_u32_e32 v46, 0x700, v22
	v_pk_add_f32 v[34:35], v[36:37], v[34:35]
	v_lshl_add_u64 v[148:149], v[22:23], 2, s[10:11]
	v_add_f32_e32 v0, v34, v35
	ds_bpermute_b32 v34, v132, v0
	v_add_u32_e32 v54, 0x14100, v48
	v_lshl_add_u64 v[156:157], v[26:27], 2, s[10:11]
	v_lshl_add_u64 v[158:159], v[28:29], 2, s[10:11]
	v_lshl_add_u64 v[150:151], v[108:109], 2, s[10:11]
	s_waitcnt lgkmcnt(0)
	v_add_f32_e32 v0, v0, v34
	ds_bpermute_b32 v34, v133, v0
	v_lshl_add_u64 v[152:153], v[106:107], 2, s[10:11]
	v_lshl_add_u64 v[154:155], v[24:25], 2, s[10:11]
	v_ashrrev_i32_e32 v111, 31, v110
	v_lshl_add_u64 v[110:111], v[110:111], 2, s[10:11]
	s_waitcnt lgkmcnt(0)
	v_add_f32_e32 v0, v0, v34
	ds_bpermute_b32 v22, v134, v0
	ds_read_b128 v[34:37], v54
	ds_read_b128 v[38:41], v54 offset:1024
	ds_read_b128 v[42:45], v54 offset:2048
	ds_read_b128 v[50:53], v54 offset:3072
	ds_read_b128 v[112:115], v54 offset:4096
	ds_read_b128 v[116:119], v54 offset:5120
	ds_read_b128 v[106:109], v54 offset:6144
	ds_read_b128 v[120:123], v54 offset:7168
	v_ashrrev_i32_e32 v47, 31, v46
	s_waitcnt lgkmcnt(8)
	v_add_f32_e32 v0, v0, v22
	ds_bpermute_b32 v22, v135, v0
	v_lshl_add_u64 v[46:47], v[46:47], 2, s[10:11]
	s_waitcnt lgkmcnt(0)
	v_add_f32_e32 v0, v0, v22
	ds_bpermute_b32 v22, v136, v0
	s_waitcnt lgkmcnt(0)
	v_add_f32_e32 v0, v0, v22
	ds_bpermute_b32 v48, v137, v0
	ds_read_b128 v[22:25], v54 offset:8192
	ds_read_b128 v[124:127], v54 offset:9216
	ds_read_b128 v[128:131], v54 offset:10240
	s_waitcnt lgkmcnt(3)
	v_add_f32_e32 v0, v0, v48
	v_fmamk_f32 v0, v0, 0x39800000, v139
	v_mul_f32_e32 v26, 0x4f800000, v0
	v_cmp_gt_f32_e32 vcc, s47, v0
	s_nop 1
	v_cndmask_b32_e32 v0, v0, v26, vcc
	v_sqrt_f32_e32 v26, v0
	s_nop 0
	v_add_u32_e32 v27, -1, v26
	v_fma_f32 v28, -v27, v26, v0
	v_cmp_ge_f32_e64 s[0:1], 0, v28
	v_add_u32_e32 v28, 1, v26
	s_nop 0
	v_cndmask_b32_e64 v27, v26, v27, s[0:1]
	v_fma_f32 v26, -v28, v26, v0
	v_cmp_lt_f32_e64 s[0:1], 0, v26
	s_nop 1
	v_cndmask_b32_e64 v26, v27, v28, s[0:1]
	v_mul_f32_e32 v27, 0x37800000, v26
	v_cndmask_b32_e32 v26, v26, v27, vcc
	v_cmp_class_f32_e32 vcc, v0, v140
	s_nop 1
	v_cndmask_b32_e32 v26, v26, v0, vcc
	v_div_scale_f32 v27, s[0:1], v26, v26, 1.0
	v_rcp_f32_e32 v28, v27
	v_mov_b32_e32 v0, v55
	s_mov_b64 s[0:1], 0
	v_fma_f32 v29, -v27, v28, 1.0
	v_fmac_f32_e32 v28, v29, v28
	v_div_scale_f32 v29, vcc, 1.0, v26, 1.0
	v_mul_f32_e32 v48, v29, v28
	v_fma_f32 v55, -v27, v48, v29
	v_fmac_f32_e32 v48, v55, v28
	v_fma_f32 v27, -v27, v48, v29
	v_div_fmas_f32 v27, v27, v28, v48
	v_div_fixup_f32 v48, v27, v26, 1.0
	v_pk_mul_f32 v[26:27], v[96:97], v[48:49] op_sel_hi:[1,0]
	v_pk_mul_f32 v[28:29], v[98:99], v[48:49] op_sel_hi:[1,0]
	v_pk_mul_f32 v[26:27], v[34:35], v[26:27]
	v_pk_mul_f32 v[28:29], v[36:37], v[28:29]
	global_store_dwordx4 v[148:149], v[26:29], off nt
	v_pk_mul_f32 v[16:17], v[16:17], v[48:49] op_sel_hi:[1,0]
	v_pk_mul_f32 v[18:19], v[18:19], v[48:49] op_sel_hi:[1,0]
	v_pk_mul_f32 v[26:27], v[94:95], v[48:49] op_sel_hi:[1,0]
	v_pk_mul_f32 v[28:29], v[92:93], v[48:49] op_sel_hi:[1,0]
	v_pk_mul_f32 v[26:27], v[38:39], v[26:27]
	v_pk_mul_f32 v[28:29], v[40:41], v[28:29]
	global_store_dwordx4 v[148:149], v[26:29], off offset:1024 nt
	v_pk_mul_f32 v[8:9], v[8:9], v[48:49] op_sel_hi:[1,0]
	v_pk_mul_f32 v[10:11], v[10:11], v[48:49] op_sel_hi:[1,0]
	v_pk_mul_f32 v[26:27], v[90:91], v[48:49] op_sel_hi:[1,0]
	v_pk_mul_f32 v[28:29], v[88:89], v[48:49] op_sel_hi:[1,0]
	v_pk_mul_f32 v[26:27], v[42:43], v[26:27]
	v_pk_mul_f32 v[28:29], v[44:45], v[28:29]
	global_store_dwordx4 v[148:149], v[26:29], off offset:2048 nt
	v_pk_mul_f32 v[0:1], v[0:1], v[48:49] op_sel_hi:[1,0]
	v_pk_mul_f32 v[2:3], v[2:3], v[48:49] op_sel_hi:[1,0]
	v_pk_mul_f32 v[26:27], v[86:87], v[48:49] op_sel_hi:[1,0]
	v_pk_mul_f32 v[28:29], v[84:85], v[48:49] op_sel_hi:[1,0]
	v_pk_mul_f32 v[26:27], v[50:51], v[26:27]
	v_pk_mul_f32 v[28:29], v[52:53], v[28:29]
	global_store_dwordx4 v[148:149], v[26:29], off offset:3072 nt
	s_and_b64 vcc, exec, s[2:3]
	s_nop 0
	v_pk_mul_f32 v[26:27], v[82:83], v[48:49] op_sel_hi:[1,0]
	v_pk_mul_f32 v[28:29], v[80:81], v[48:49] op_sel_hi:[1,0]
	v_pk_mul_f32 v[26:27], v[112:113], v[26:27]
	v_pk_mul_f32 v[28:29], v[114:115], v[28:29]
	global_store_dwordx4 v[150:151], v[26:29], off nt
	s_nop 1
	v_pk_mul_f32 v[26:27], v[78:79], v[48:49] op_sel_hi:[1,0]
	v_pk_mul_f32 v[28:29], v[76:77], v[48:49] op_sel_hi:[1,0]
	v_pk_mul_f32 v[26:27], v[116:117], v[26:27]
	v_pk_mul_f32 v[28:29], v[118:119], v[28:29]
	global_store_dwordx4 v[152:153], v[26:29], off nt
	s_nop 1
	v_pk_mul_f32 v[26:27], v[74:75], v[48:49] op_sel_hi:[1,0]
	v_pk_mul_f32 v[28:29], v[72:73], v[48:49] op_sel_hi:[1,0]
	v_pk_mul_f32 v[26:27], v[26:27], v[106:107]
	v_pk_mul_f32 v[28:29], v[28:29], v[108:109]
	global_store_dwordx4 v[110:111], v[26:29], off nt
	s_nop 1
	v_pk_mul_f32 v[26:27], v[70:71], v[48:49] op_sel_hi:[1,0]
	v_pk_mul_f32 v[28:29], v[68:69], v[48:49] op_sel_hi:[1,0]
	v_pk_mul_f32 v[26:27], v[26:27], v[120:121]
	v_pk_mul_f32 v[28:29], v[28:29], v[122:123]
	global_store_dwordx4 v[46:47], v[26:29], off nt
	s_nop 1
	v_pk_mul_f32 v[26:27], v[66:67], v[48:49] op_sel_hi:[1,0]
	v_pk_mul_f32 v[28:29], v[64:65], v[48:49] op_sel_hi:[1,0]
	s_waitcnt lgkmcnt(2)
	v_pk_mul_f32 v[22:23], v[26:27], v[22:23]
	v_pk_mul_f32 v[24:25], v[28:29], v[24:25]
	global_store_dwordx4 v[154:155], v[22:25], off nt
	v_pk_mul_f32 v[26:27], v[58:59], v[48:49] op_sel_hi:[1,0]
	v_pk_mul_f32 v[28:29], v[56:57], v[48:49] op_sel_hi:[1,0]
	v_pk_mul_f32 v[22:23], v[62:63], v[48:49] op_sel_hi:[1,0]
	v_pk_mul_f32 v[24:25], v[60:61], v[48:49] op_sel_hi:[1,0]
	s_waitcnt lgkmcnt(1)
	v_pk_mul_f32 v[22:23], v[22:23], v[124:125]
	v_pk_mul_f32 v[24:25], v[24:25], v[126:127]
	global_store_dwordx4 v[156:157], v[22:25], off nt
	ds_read_b128 v[22:25], v54 offset:11264
	s_waitcnt lgkmcnt(1)
	v_pk_mul_f32 v[28:29], v[28:29], v[130:131]
	v_pk_mul_f32 v[26:27], v[26:27], v[128:129]
	global_store_dwordx4 v[158:159], v[26:29], off nt
	s_waitcnt lgkmcnt(0)
	v_pk_mul_f32 v[18:19], v[18:19], v[24:25]
	v_pk_mul_f32 v[16:17], v[16:17], v[22:23]
	ds_read_b128 v[22:25], v54 offset:12288
	global_store_dwordx4 v[30:31], v[16:19], off nt
	s_nop 1
	v_pk_mul_f32 v[16:17], v[12:13], v[48:49] op_sel_hi:[1,0]
	v_pk_mul_f32 v[18:19], v[14:15], v[48:49] op_sel_hi:[1,0]
	ds_read_b128 v[12:15], v54 offset:13312
	s_waitcnt lgkmcnt(1)
	v_pk_mul_f32 v[18:19], v[18:19], v[24:25]
	v_pk_mul_f32 v[16:17], v[16:17], v[22:23]
	global_store_dwordx4 v[102:103], v[16:19], off nt
	s_waitcnt lgkmcnt(0)
	v_pk_mul_f32 v[10:11], v[10:11], v[14:15]
	v_pk_mul_f32 v[8:9], v[8:9], v[12:13]
	ds_read_b128 v[12:15], v54 offset:14336
	global_store_dwordx4 v[100:101], v[8:11], off nt
	s_nop 1
	v_pk_mul_f32 v[10:11], v[6:7], v[48:49] op_sel_hi:[1,0]
	v_pk_mul_f32 v[8:9], v[4:5], v[48:49] op_sel_hi:[1,0]
	ds_read_b128 v[4:7], v54 offset:15360
	s_waitcnt lgkmcnt(1)
	v_pk_mul_f32 v[8:9], v[8:9], v[12:13]
	v_pk_mul_f32 v[10:11], v[10:11], v[14:15]
	global_store_dwordx4 v[104:105], v[8:11], off nt
	s_waitcnt lgkmcnt(0)
	v_pk_mul_f32 v[0:1], v[0:1], v[4:5]
	v_pk_mul_f32 v[2:3], v[2:3], v[6:7]
	v_lshl_add_u64 v[4:5], v[20:21], 2, s[10:11]
	global_store_dwordx4 v[4:5], v[0:3], off nt
	s_cbranch_vccz .LBB0_1584
	s_add_i32 s77, s77, s97
	s_cmpk_gt_i32 s77, 0x1ff
	s_barrier
	s_cbranch_scc0 .LBB0_1498
